# down GEMM: L2 prefetch of the next unit's A tile from the epilogue start (3 dword loads per wave) with counted waits adjusted; down epilogue wait fix; final RMSNorm rewrite
# baseline (speedup 1.0000x reference)
.LBB0_1623:
	s_ashr_i32 s41, s40, 31
	s_lshl_b64 s[8:9], s[40:41], 18
	s_add_u32 s44, s33, s8
	ds_read_b128 v[10:13], v162
	ds_read_b128 v[14:17], v162 offset:1024
	ds_read_b128 v[26:29], v162 offset:2048
	ds_read_b128 v[30:33], v162 offset:3072
	ds_read_b128 v[172:175], v163
	ds_read_b128 v[176:179], v163 offset:1024
	ds_read_b128 v[180:183], v163 offset:2048
	ds_read_b128 v[184:187], v163 offset:3072
	s_addc_u32 s45, s37, s9
	s_and_b64 s[8:9], s[6:7], exec
	s_cselect_b32 s75, s45, s69
	s_cselect_b32 s74, s44, s68
	s_ashr_i32 s43, s42, 31
	s_ashr_i32 s39, s38, 31
	s_lshl_b64 s[8:9], s[42:43], 20
	s_lshl_b64 s[46:47], s[38:39], 18
	s_add_u32 s8, s54, s8
	s_addc_u32 s9, s55, s9
	s_add_u32 s46, s8, s46
	s_addc_u32 s47, s9, s47
	s_and_b64 s[8:9], s[6:7], exec
	s_cselect_b32 s9, s47, s73
	s_cselect_b32 s8, s46, s72
	ds_read_b128 v[18:21], v161
	ds_read_b128 v[22:25], v161 offset:1024
	ds_read_b128 v[34:37], v161 offset:2048
	ds_read_b128 v[38:41], v161 offset:3072
	ds_read_b128 v[42:45], v161 offset:4096
	ds_read_b128 v[46:49], v161 offset:5120
	ds_read_b128 v[50:53], v161 offset:6144
	ds_read_b128 v[54:57], v161 offset:7168
	s_waitcnt vmcnt(29)
	s_waitcnt lgkmcnt(0)
	s_barrier
	s_setprio 1
	s_waitcnt lgkmcnt(0)
	v_mfma_f32_16x16x128_f8f6f4 v[134:137], v[10:17], v[18:25], 0
	v_mfma_f32_16x16x128_f8f6f4 v[130:133], v[26:33], v[18:25], 0
	v_mfma_f32_16x16x128_f8f6f4 v[118:121], v[10:17], v[34:41], 0
	v_mfma_f32_16x16x128_f8f6f4 v[114:117], v[26:33], v[34:41], 0
	v_mfma_f32_16x16x128_f8f6f4 v[102:105], v[10:17], v[42:49], 0
	v_mfma_f32_16x16x128_f8f6f4 v[98:101], v[26:33], v[42:49], 0
	v_mfma_f32_16x16x128_f8f6f4 v[78:81], v[10:17], v[50:57], 0
	v_mfma_f32_16x16x128_f8f6f4 v[74:77], v[26:33], v[50:57], 0
	s_setprio 0
	s_setprio 1
	v_mfma_f32_16x16x128_f8f6f4 v[126:129], v[172:179], v[18:25], 0
	v_mfma_f32_16x16x128_f8f6f4 v[122:125], v[180:187], v[18:25], 0
	v_mfma_f32_16x16x128_f8f6f4 v[110:113], v[172:179], v[34:41], 0
	v_mfma_f32_16x16x128_f8f6f4 v[106:109], v[180:187], v[34:41], 0
	v_mfma_f32_16x16x128_f8f6f4 v[94:97], v[172:179], v[42:49], 0
	v_mfma_f32_16x16x128_f8f6f4 v[90:93], v[180:187], v[42:49], 0
	v_mfma_f32_16x16x128_f8f6f4 v[62:65], v[172:179], v[50:57], 0
	v_mfma_f32_16x16x128_f8f6f4 v[58:61], v[180:187], v[50:57], 0
	s_setprio 0
	s_barrier
	s_add_i32 s80, s66, s58
	v_lshl_add_u64 v[150:151], s[72:73], 0, v[140:141]
	s_add_i32 s76, s80, 0x2000
	v_lshl_add_u64 v[18:19], v[150:151], 0, s[22:23]
	s_mov_b32 m0, s80
	v_lshl_add_u64 v[152:153], s[72:73], 0, v[144:145]
	s_add_u32 s78, s72, 0x8100
	ds_read_b128 v[42:45], v161 offset:16384
	ds_read_b128 v[46:49], v161 offset:17408
	ds_read_b128 v[188:191], v161 offset:18432
	ds_read_b128 v[192:195], v161 offset:19456
	ds_read_b128 v[204:207], v161 offset:20480
	ds_read_b128 v[208:211], v161 offset:21504
	ds_read_b128 v[212:215], v161 offset:22528
	ds_read_b128 v[216:219], v161 offset:23552
	global_load_lds_dwordx4 v[18:19], off
	v_lshl_add_u64 v[18:19], v[152:153], 0, s[22:23]
	s_mov_b32 m0, s76
	s_addc_u32 s79, s73, 0
	s_add_i32 s77, s67, s58
	global_load_lds_dwordx4 v[18:19], off
	v_lshl_add_u64 v[18:19], s[78:79], 0, v[140:141]
	s_mov_b32 m0, s77
	v_lshl_add_u64 v[154:155], s[68:69], 0, v[138:139]
	global_load_lds_dwordx4 v[18:19], off
	v_lshl_add_u64 v[18:19], s[78:79], 0, v[144:145]
	s_add_i32 s78, s77, 0x2000
	s_mov_b32 m0, s78
	v_lshl_add_u64 v[156:157], s[68:69], 0, v[142:143]
	global_load_lds_dwordx4 v[18:19], off
	v_lshl_add_u64 v[18:19], v[154:155], 0, s[22:23]
	s_mov_b32 m0, s49
	s_nop 0
	global_load_lds_dwordx4 v[18:19], off
	v_lshl_add_u64 v[18:19], v[156:157], 0, s[22:23]
	s_mov_b32 m0, s51
	s_nop 0
	global_load_lds_dwordx4 v[18:19], off
	s_waitcnt vmcnt(29)
	s_waitcnt lgkmcnt(0)
	s_barrier
	s_setprio 1
	s_waitcnt lgkmcnt(0)
	v_mfma_f32_16x16x128_f8f6f4 v[86:89], v[10:17], v[42:49], 0
	v_mfma_f32_16x16x128_f8f6f4 v[82:85], v[26:33], v[42:49], 0
	v_mfma_f32_16x16x128_f8f6f4 v[54:57], v[10:17], v[188:195], 0
	v_mfma_f32_16x16x128_f8f6f4 v[50:53], v[26:33], v[188:195], 0
	v_mfma_f32_16x16x128_f8f6f4 v[38:41], v[10:17], v[204:211], 0
	v_mfma_f32_16x16x128_f8f6f4 v[34:37], v[26:33], v[204:211], 0
	v_mfma_f32_16x16x128_f8f6f4 v[22:25], v[10:17], v[212:219], 0
	v_mfma_f32_16x16x128_f8f6f4 v[18:21], v[26:33], v[212:219], 0
	s_setprio 0
	s_setprio 1
	v_mfma_f32_16x16x128_f8f6f4 v[70:73], v[172:179], v[42:49], 0
	v_mfma_f32_16x16x128_f8f6f4 v[66:69], v[180:187], v[42:49], 0
	v_mfma_f32_16x16x128_f8f6f4 v[46:49], v[172:179], v[188:195], 0
	v_mfma_f32_16x16x128_f8f6f4 v[42:45], v[180:187], v[188:195], 0
	v_mfma_f32_16x16x128_f8f6f4 v[30:33], v[172:179], v[204:211], 0
	v_mfma_f32_16x16x128_f8f6f4 v[26:29], v[180:187], v[204:211], 0
	v_mfma_f32_16x16x128_f8f6f4 v[14:17], v[172:179], v[212:219], 0
	v_mfma_f32_16x16x128_f8f6f4 v[10:13], v[180:187], v[212:219], 0
	s_setprio 0
	s_barrier
	s_add_i32 s79, 0, 0x18000
	s_add_i32 s41, 0, 0x1c000
	v_add_u32_e32 v158, s79, v160
	v_add_u32_e32 v159, s41, v160
	ds_read_b128 v[172:175], v158
	ds_read_b128 v[176:179], v158 offset:1024
	ds_read_b128 v[180:183], v158 offset:2048
	ds_read_b128 v[184:187], v158 offset:3072
	ds_read_b128 v[188:191], v159
	ds_read_b128 v[192:195], v159 offset:1024
	ds_read_b128 v[204:207], v159 offset:2048
	ds_read_b128 v[208:211], v159 offset:3072
	s_add_u32 s82, s68, 0x20100
	s_addc_u32 s83, s69, 0
	s_mov_b32 m0, s59
	v_lshl_add_u64 v[196:197], s[82:83], 0, v[138:139]
	ds_read_b128 v[212:215], v161 offset:32768
	ds_read_b128 v[216:219], v161 offset:33792
	ds_read_b128 v[220:223], v161 offset:34816
	ds_read_b128 v[224:227], v161 offset:35840
	ds_read_b128 v[228:231], v161 offset:36864
	ds_read_b128 v[232:235], v161 offset:37888
	ds_read_b128 v[236:239], v161 offset:38912
	ds_read_b128 v[240:243], v161 offset:39936
	global_load_lds_dwordx4 v[196:197], off
	v_lshl_add_u64 v[196:197], s[82:83], 0, v[142:143]
	s_mov_b32 m0, s60
	s_nop 0
	global_load_lds_dwordx4 v[196:197], off
	s_waitcnt vmcnt(29)
	s_waitcnt lgkmcnt(0)
	s_barrier
	s_setprio 1
	s_waitcnt lgkmcnt(0)
	v_mfma_f32_16x16x128_f8f6f4 v[134:137], v[172:179], v[212:219], v[134:137]
	v_mfma_f32_16x16x128_f8f6f4 v[130:133], v[180:187], v[212:219], v[130:133]
	v_mfma_f32_16x16x128_f8f6f4 v[118:121], v[172:179], v[220:227], v[118:121]
	v_mfma_f32_16x16x128_f8f6f4 v[114:117], v[180:187], v[220:227], v[114:117]
	v_mfma_f32_16x16x128_f8f6f4 v[102:105], v[172:179], v[228:235], v[102:105]
	v_mfma_f32_16x16x128_f8f6f4 v[98:101], v[180:187], v[228:235], v[98:101]
	v_mfma_f32_16x16x128_f8f6f4 v[78:81], v[172:179], v[236:243], v[78:81]
	v_mfma_f32_16x16x128_f8f6f4 v[74:77], v[180:187], v[236:243], v[74:77]
	s_setprio 0
	s_setprio 1
	v_mfma_f32_16x16x128_f8f6f4 v[126:129], v[188:195], v[212:219], v[126:129]
	v_mfma_f32_16x16x128_f8f6f4 v[122:125], v[204:211], v[212:219], v[122:125]
	v_mfma_f32_16x16x128_f8f6f4 v[110:113], v[188:195], v[220:227], v[110:113]
	v_mfma_f32_16x16x128_f8f6f4 v[106:109], v[204:211], v[220:227], v[106:109]
	v_mfma_f32_16x16x128_f8f6f4 v[94:97], v[188:195], v[228:235], v[94:97]
	v_mfma_f32_16x16x128_f8f6f4 v[90:93], v[204:211], v[228:235], v[90:93]
	v_mfma_f32_16x16x128_f8f6f4 v[62:65], v[188:195], v[236:243], v[62:65]
	v_mfma_f32_16x16x128_f8f6f4 v[58:61], v[204:211], v[236:243], v[58:61]
	s_setprio 0
	s_barrier
	s_add_i32 s79, s79, s58
	s_add_i32 s39, s79, 0x2000
	v_lshl_add_u64 v[196:197], v[150:151], 0, s[24:25]
	s_mov_b32 m0, s79
	s_add_u32 s82, s72, 0x8180
	ds_read_b128 v[212:215], v161 offset:49152
	ds_read_b128 v[216:219], v161 offset:50176
	ds_read_b128 v[220:223], v161 offset:51200
	ds_read_b128 v[224:227], v161 offset:52224
	ds_read_b128 v[228:231], v161 offset:53248
	ds_read_b128 v[232:235], v161 offset:54272
	ds_read_b128 v[236:239], v161 offset:55296
	ds_read_b128 v[240:243], v161 offset:56320
	global_load_lds_dwordx4 v[196:197], off
	v_lshl_add_u64 v[196:197], v[152:153], 0, s[24:25]
	s_mov_b32 m0, s39
	s_addc_u32 s83, s73, 0
	s_add_i32 s41, s41, s58
	global_load_lds_dwordx4 v[196:197], off
	v_lshl_add_u64 v[196:197], s[82:83], 0, v[140:141]
	s_mov_b32 m0, s41
	s_add_i32 s71, s41, 0x2000
	global_load_lds_dwordx4 v[196:197], off
	v_lshl_add_u64 v[196:197], s[82:83], 0, v[144:145]
	s_mov_b32 m0, s71
	s_nop 0
	global_load_lds_dwordx4 v[196:197], off
	v_lshl_add_u64 v[196:197], v[154:155], 0, s[24:25]
	s_mov_b32 m0, s61
	s_nop 0
	global_load_lds_dwordx4 v[196:197], off
	v_lshl_add_u64 v[196:197], v[156:157], 0, s[24:25]
	s_mov_b32 m0, s62
	s_nop 0
	global_load_lds_dwordx4 v[196:197], off
	s_waitcnt vmcnt(8)
	s_waitcnt lgkmcnt(0)
	s_barrier
	s_setprio 1
	s_waitcnt lgkmcnt(0)
	v_mfma_f32_16x16x128_f8f6f4 v[86:89], v[172:179], v[212:219], v[86:89]
	v_mfma_f32_16x16x128_f8f6f4 v[82:85], v[180:187], v[212:219], v[82:85]
	v_mfma_f32_16x16x128_f8f6f4 v[54:57], v[172:179], v[220:227], v[54:57]
	v_mfma_f32_16x16x128_f8f6f4 v[50:53], v[180:187], v[220:227], v[50:53]
	v_mfma_f32_16x16x128_f8f6f4 v[38:41], v[172:179], v[228:235], v[38:41]
	v_mfma_f32_16x16x128_f8f6f4 v[34:37], v[180:187], v[228:235], v[34:37]
	v_mfma_f32_16x16x128_f8f6f4 v[22:25], v[172:179], v[236:243], v[22:25]
	v_mfma_f32_16x16x128_f8f6f4 v[18:21], v[180:187], v[236:243], v[18:21]
	s_setprio 0
	s_setprio 1
	v_mfma_f32_16x16x128_f8f6f4 v[70:73], v[188:195], v[212:219], v[70:73]
	v_mfma_f32_16x16x128_f8f6f4 v[66:69], v[204:211], v[212:219], v[66:69]
	v_mfma_f32_16x16x128_f8f6f4 v[46:49], v[188:195], v[220:227], v[46:49]
	v_mfma_f32_16x16x128_f8f6f4 v[42:45], v[204:211], v[220:227], v[42:45]
	v_mfma_f32_16x16x128_f8f6f4 v[30:33], v[188:195], v[228:235], v[30:33]
	v_mfma_f32_16x16x128_f8f6f4 v[26:29], v[204:211], v[228:235], v[26:29]
	v_mfma_f32_16x16x128_f8f6f4 v[14:17], v[188:195], v[236:243], v[14:17]
	v_mfma_f32_16x16x128_f8f6f4 v[10:13], v[204:211], v[236:243], v[10:13]
	s_setprio 0
	s_barrier
	ds_read_b128 v[172:175], v162
	ds_read_b128 v[176:179], v162 offset:1024
	ds_read_b128 v[180:183], v162 offset:2048
	ds_read_b128 v[184:187], v162 offset:3072
	ds_read_b128 v[188:191], v163
	ds_read_b128 v[192:195], v163 offset:1024
	ds_read_b128 v[204:207], v163 offset:2048
	ds_read_b128 v[208:211], v163 offset:3072
	s_add_u32 s82, s68, 0x20180
	s_addc_u32 s83, s69, 0
	s_mov_b32 m0, s63
	v_lshl_add_u64 v[196:197], s[82:83], 0, v[138:139]
	ds_read_b128 v[212:215], v161
	ds_read_b128 v[216:219], v161 offset:1024
	ds_read_b128 v[220:223], v161 offset:2048
	ds_read_b128 v[224:227], v161 offset:3072
	ds_read_b128 v[228:231], v161 offset:4096
	ds_read_b128 v[232:235], v161 offset:5120
	ds_read_b128 v[236:239], v161 offset:6144
	ds_read_b128 v[240:243], v161 offset:7168
	global_load_lds_dwordx4 v[196:197], off
	v_lshl_add_u64 v[196:197], s[82:83], 0, v[142:143]
	s_mov_b32 m0, s64
	s_nop 0
	global_load_lds_dwordx4 v[196:197], off
	s_waitcnt vmcnt(8)
	s_waitcnt lgkmcnt(0)
	s_barrier
	s_setprio 1
	s_waitcnt lgkmcnt(0)
	v_mfma_f32_16x16x128_f8f6f4 v[134:137], v[172:179], v[212:219], v[134:137]
	v_mfma_f32_16x16x128_f8f6f4 v[130:133], v[180:187], v[212:219], v[130:133]
	v_mfma_f32_16x16x128_f8f6f4 v[118:121], v[172:179], v[220:227], v[118:121]
	v_mfma_f32_16x16x128_f8f6f4 v[114:117], v[180:187], v[220:227], v[114:117]
	v_mfma_f32_16x16x128_f8f6f4 v[102:105], v[172:179], v[228:235], v[102:105]
	v_mfma_f32_16x16x128_f8f6f4 v[98:101], v[180:187], v[228:235], v[98:101]
	v_mfma_f32_16x16x128_f8f6f4 v[78:81], v[172:179], v[236:243], v[78:81]
	v_mfma_f32_16x16x128_f8f6f4 v[74:77], v[180:187], v[236:243], v[74:77]
	s_setprio 0
	s_setprio 1
	v_mfma_f32_16x16x128_f8f6f4 v[126:129], v[188:195], v[212:219], v[126:129]
	v_mfma_f32_16x16x128_f8f6f4 v[122:125], v[204:211], v[212:219], v[122:125]
	v_mfma_f32_16x16x128_f8f6f4 v[110:113], v[188:195], v[220:227], v[110:113]
	v_mfma_f32_16x16x128_f8f6f4 v[106:109], v[204:211], v[220:227], v[106:109]
	v_mfma_f32_16x16x128_f8f6f4 v[94:97], v[188:195], v[228:235], v[94:97]
	v_mfma_f32_16x16x128_f8f6f4 v[90:93], v[204:211], v[228:235], v[90:93]
	v_mfma_f32_16x16x128_f8f6f4 v[62:65], v[188:195], v[236:243], v[62:65]
	v_mfma_f32_16x16x128_f8f6f4 v[58:61], v[204:211], v[236:243], v[58:61]
	s_setprio 0
	s_barrier
	s_mov_b32 m0, s80
	v_lshl_add_u64 v[196:197], v[150:151], 0, s[26:27]
	s_add_u32 s82, s72, 0x8200
	ds_read_b128 v[212:215], v161 offset:16384
	ds_read_b128 v[216:219], v161 offset:17408
	ds_read_b128 v[220:223], v161 offset:18432
	ds_read_b128 v[224:227], v161 offset:19456
	ds_read_b128 v[228:231], v161 offset:20480
	ds_read_b128 v[232:235], v161 offset:21504
	ds_read_b128 v[236:239], v161 offset:22528
	ds_read_b128 v[240:243], v161 offset:23552
	global_load_lds_dwordx4 v[196:197], off
	v_lshl_add_u64 v[196:197], v[152:153], 0, s[26:27]
	s_mov_b32 m0, s76
	s_addc_u32 s83, s73, 0
	global_load_lds_dwordx4 v[196:197], off
	v_lshl_add_u64 v[196:197], s[82:83], 0, v[140:141]
	s_mov_b32 m0, s77
	s_nop 0
	global_load_lds_dwordx4 v[196:197], off
	v_lshl_add_u64 v[196:197], s[82:83], 0, v[144:145]
	s_mov_b32 m0, s78
	s_nop 0
	global_load_lds_dwordx4 v[196:197], off
	v_lshl_add_u64 v[196:197], v[154:155], 0, s[26:27]
	s_mov_b32 m0, s49
	s_nop 0
	global_load_lds_dwordx4 v[196:197], off
	v_lshl_add_u64 v[196:197], v[156:157], 0, s[26:27]
	s_mov_b32 m0, s51
	s_nop 0
	global_load_lds_dwordx4 v[196:197], off
	s_waitcnt vmcnt(8)
	s_waitcnt lgkmcnt(0)
	s_barrier
	s_setprio 1
	s_waitcnt lgkmcnt(0)
	v_mfma_f32_16x16x128_f8f6f4 v[86:89], v[172:179], v[212:219], v[86:89]
	v_mfma_f32_16x16x128_f8f6f4 v[82:85], v[180:187], v[212:219], v[82:85]
	v_mfma_f32_16x16x128_f8f6f4 v[54:57], v[172:179], v[220:227], v[54:57]
	v_mfma_f32_16x16x128_f8f6f4 v[50:53], v[180:187], v[220:227], v[50:53]
	v_mfma_f32_16x16x128_f8f6f4 v[38:41], v[172:179], v[228:235], v[38:41]
	v_mfma_f32_16x16x128_f8f6f4 v[34:37], v[180:187], v[228:235], v[34:37]
	v_mfma_f32_16x16x128_f8f6f4 v[22:25], v[172:179], v[236:243], v[22:25]
	v_mfma_f32_16x16x128_f8f6f4 v[18:21], v[180:187], v[236:243], v[18:21]
	s_setprio 0
	s_setprio 1
	v_mfma_f32_16x16x128_f8f6f4 v[70:73], v[188:195], v[212:219], v[70:73]
	v_mfma_f32_16x16x128_f8f6f4 v[66:69], v[204:211], v[212:219], v[66:69]
	v_mfma_f32_16x16x128_f8f6f4 v[46:49], v[188:195], v[220:227], v[46:49]
	v_mfma_f32_16x16x128_f8f6f4 v[42:45], v[204:211], v[220:227], v[42:45]
	v_mfma_f32_16x16x128_f8f6f4 v[30:33], v[188:195], v[228:235], v[30:33]
	v_mfma_f32_16x16x128_f8f6f4 v[26:29], v[204:211], v[228:235], v[26:29]
	v_mfma_f32_16x16x128_f8f6f4 v[14:17], v[188:195], v[236:243], v[14:17]
	v_mfma_f32_16x16x128_f8f6f4 v[10:13], v[204:211], v[236:243], v[10:13]
	s_setprio 0
	s_barrier
	ds_read_b128 v[172:175], v158
	ds_read_b128 v[176:179], v158 offset:1024
	ds_read_b128 v[180:183], v158 offset:2048
	ds_read_b128 v[184:187], v158 offset:3072
	ds_read_b128 v[188:191], v159
	ds_read_b128 v[192:195], v159 offset:1024
	ds_read_b128 v[204:207], v159 offset:2048
	ds_read_b128 v[208:211], v159 offset:3072
	s_add_u32 s82, s68, 0x20200
	s_addc_u32 s83, s69, 0
	s_mov_b32 m0, s59
	v_lshl_add_u64 v[196:197], s[82:83], 0, v[138:139]
	ds_read_b128 v[212:215], v161 offset:32768
	ds_read_b128 v[216:219], v161 offset:33792
	ds_read_b128 v[220:223], v161 offset:34816
	ds_read_b128 v[224:227], v161 offset:35840
	ds_read_b128 v[228:231], v161 offset:36864
	ds_read_b128 v[232:235], v161 offset:37888
	ds_read_b128 v[236:239], v161 offset:38912
	ds_read_b128 v[240:243], v161 offset:39936
	global_load_lds_dwordx4 v[196:197], off
	v_lshl_add_u64 v[196:197], s[82:83], 0, v[142:143]
	s_mov_b32 m0, s60
	s_nop 0
	global_load_lds_dwordx4 v[196:197], off
	s_waitcnt vmcnt(8)
	s_waitcnt lgkmcnt(0)
	s_barrier
	s_setprio 1
	s_waitcnt lgkmcnt(0)
	v_mfma_f32_16x16x128_f8f6f4 v[134:137], v[172:179], v[212:219], v[134:137]
	v_mfma_f32_16x16x128_f8f6f4 v[130:133], v[180:187], v[212:219], v[130:133]
	v_mfma_f32_16x16x128_f8f6f4 v[118:121], v[172:179], v[220:227], v[118:121]
	v_mfma_f32_16x16x128_f8f6f4 v[114:117], v[180:187], v[220:227], v[114:117]
	v_mfma_f32_16x16x128_f8f6f4 v[102:105], v[172:179], v[228:235], v[102:105]
	v_mfma_f32_16x16x128_f8f6f4 v[98:101], v[180:187], v[228:235], v[98:101]
	v_mfma_f32_16x16x128_f8f6f4 v[78:81], v[172:179], v[236:243], v[78:81]
	v_mfma_f32_16x16x128_f8f6f4 v[74:77], v[180:187], v[236:243], v[74:77]
	s_setprio 0
	s_setprio 1
	v_mfma_f32_16x16x128_f8f6f4 v[126:129], v[188:195], v[212:219], v[126:129]
	v_mfma_f32_16x16x128_f8f6f4 v[122:125], v[204:211], v[212:219], v[122:125]
	v_mfma_f32_16x16x128_f8f6f4 v[110:113], v[188:195], v[220:227], v[110:113]
	v_mfma_f32_16x16x128_f8f6f4 v[106:109], v[204:211], v[220:227], v[106:109]
	v_mfma_f32_16x16x128_f8f6f4 v[94:97], v[188:195], v[228:235], v[94:97]
	v_mfma_f32_16x16x128_f8f6f4 v[90:93], v[204:211], v[228:235], v[90:93]
	v_mfma_f32_16x16x128_f8f6f4 v[62:65], v[188:195], v[236:243], v[62:65]
	v_mfma_f32_16x16x128_f8f6f4 v[58:61], v[204:211], v[236:243], v[58:61]
	s_setprio 0
	s_barrier
	s_mov_b32 m0, s79
	v_lshl_add_u64 v[196:197], v[150:151], 0, s[28:29]
	s_add_u32 s82, s72, 0x8280
	ds_read_b128 v[212:215], v161 offset:49152
	ds_read_b128 v[216:219], v161 offset:50176
	ds_read_b128 v[220:223], v161 offset:51200
	ds_read_b128 v[224:227], v161 offset:52224
	ds_read_b128 v[228:231], v161 offset:53248
	ds_read_b128 v[232:235], v161 offset:54272
	ds_read_b128 v[236:239], v161 offset:55296
	ds_read_b128 v[240:243], v161 offset:56320
	global_load_lds_dwordx4 v[196:197], off
	v_lshl_add_u64 v[196:197], v[152:153], 0, s[28:29]
	s_mov_b32 m0, s39
	s_addc_u32 s83, s73, 0
	global_load_lds_dwordx4 v[196:197], off
	v_lshl_add_u64 v[196:197], s[82:83], 0, v[140:141]
	s_mov_b32 m0, s41
	s_nop 0
	global_load_lds_dwordx4 v[196:197], off
	v_lshl_add_u64 v[196:197], s[82:83], 0, v[144:145]
	s_mov_b32 m0, s71
	s_nop 0
	global_load_lds_dwordx4 v[196:197], off
	v_lshl_add_u64 v[196:197], v[154:155], 0, s[28:29]
	s_mov_b32 m0, s61
	s_nop 0
	global_load_lds_dwordx4 v[196:197], off
	v_lshl_add_u64 v[196:197], v[156:157], 0, s[28:29]
	s_mov_b32 m0, s62
	s_nop 0
	global_load_lds_dwordx4 v[196:197], off
	s_waitcnt vmcnt(8)
	s_waitcnt lgkmcnt(0)
	s_barrier
	s_setprio 1
	s_waitcnt lgkmcnt(0)
	v_mfma_f32_16x16x128_f8f6f4 v[86:89], v[172:179], v[212:219], v[86:89]
	v_mfma_f32_16x16x128_f8f6f4 v[82:85], v[180:187], v[212:219], v[82:85]
	v_mfma_f32_16x16x128_f8f6f4 v[54:57], v[172:179], v[220:227], v[54:57]
	v_mfma_f32_16x16x128_f8f6f4 v[50:53], v[180:187], v[220:227], v[50:53]
	v_mfma_f32_16x16x128_f8f6f4 v[38:41], v[172:179], v[228:235], v[38:41]
	v_mfma_f32_16x16x128_f8f6f4 v[34:37], v[180:187], v[228:235], v[34:37]
	v_mfma_f32_16x16x128_f8f6f4 v[22:25], v[172:179], v[236:243], v[22:25]
	v_mfma_f32_16x16x128_f8f6f4 v[18:21], v[180:187], v[236:243], v[18:21]
	s_setprio 0
	s_setprio 1
	v_mfma_f32_16x16x128_f8f6f4 v[70:73], v[188:195], v[212:219], v[70:73]
	v_mfma_f32_16x16x128_f8f6f4 v[66:69], v[204:211], v[212:219], v[66:69]
	v_mfma_f32_16x16x128_f8f6f4 v[46:49], v[188:195], v[220:227], v[46:49]
	v_mfma_f32_16x16x128_f8f6f4 v[42:45], v[204:211], v[220:227], v[42:45]
	v_mfma_f32_16x16x128_f8f6f4 v[30:33], v[188:195], v[228:235], v[30:33]
	v_mfma_f32_16x16x128_f8f6f4 v[26:29], v[204:211], v[228:235], v[26:29]
	v_mfma_f32_16x16x128_f8f6f4 v[14:17], v[188:195], v[236:243], v[14:17]
	v_mfma_f32_16x16x128_f8f6f4 v[10:13], v[204:211], v[236:243], v[10:13]
	s_setprio 0
	s_barrier
	ds_read_b128 v[172:175], v162
	ds_read_b128 v[176:179], v162 offset:1024
	ds_read_b128 v[180:183], v162 offset:2048
	ds_read_b128 v[184:187], v162 offset:3072
	ds_read_b128 v[188:191], v163
	ds_read_b128 v[192:195], v163 offset:1024
	ds_read_b128 v[204:207], v163 offset:2048
	ds_read_b128 v[208:211], v163 offset:3072
	s_add_u32 s82, s68, 0x20280
	s_addc_u32 s83, s69, 0
	s_mov_b32 m0, s63
	v_lshl_add_u64 v[196:197], s[82:83], 0, v[138:139]
	ds_read_b128 v[212:215], v161
	ds_read_b128 v[216:219], v161 offset:1024
	ds_read_b128 v[220:223], v161 offset:2048
	ds_read_b128 v[224:227], v161 offset:3072
	ds_read_b128 v[228:231], v161 offset:4096
	ds_read_b128 v[232:235], v161 offset:5120
	ds_read_b128 v[236:239], v161 offset:6144
	ds_read_b128 v[240:243], v161 offset:7168
	global_load_lds_dwordx4 v[196:197], off
	v_lshl_add_u64 v[196:197], s[82:83], 0, v[142:143]
	s_mov_b32 m0, s64
	s_nop 0
	global_load_lds_dwordx4 v[196:197], off
	s_waitcnt vmcnt(8)
	s_waitcnt lgkmcnt(0)
	s_barrier
	s_setprio 1
	s_waitcnt lgkmcnt(0)
	v_mfma_f32_16x16x128_f8f6f4 v[134:137], v[172:179], v[212:219], v[134:137]
	v_mfma_f32_16x16x128_f8f6f4 v[130:133], v[180:187], v[212:219], v[130:133]
	v_mfma_f32_16x16x128_f8f6f4 v[118:121], v[172:179], v[220:227], v[118:121]
	v_mfma_f32_16x16x128_f8f6f4 v[114:117], v[180:187], v[220:227], v[114:117]
	v_mfma_f32_16x16x128_f8f6f4 v[102:105], v[172:179], v[228:235], v[102:105]
	v_mfma_f32_16x16x128_f8f6f4 v[98:101], v[180:187], v[228:235], v[98:101]
	v_mfma_f32_16x16x128_f8f6f4 v[78:81], v[172:179], v[236:243], v[78:81]
	v_mfma_f32_16x16x128_f8f6f4 v[74:77], v[180:187], v[236:243], v[74:77]
	s_setprio 0
	s_setprio 1
	v_mfma_f32_16x16x128_f8f6f4 v[126:129], v[188:195], v[212:219], v[126:129]
	v_mfma_f32_16x16x128_f8f6f4 v[122:125], v[204:211], v[212:219], v[122:125]
	v_mfma_f32_16x16x128_f8f6f4 v[110:113], v[188:195], v[220:227], v[110:113]
	v_mfma_f32_16x16x128_f8f6f4 v[106:109], v[204:211], v[220:227], v[106:109]
	v_mfma_f32_16x16x128_f8f6f4 v[94:97], v[188:195], v[228:235], v[94:97]
	v_mfma_f32_16x16x128_f8f6f4 v[90:93], v[204:211], v[228:235], v[90:93]
	v_mfma_f32_16x16x128_f8f6f4 v[62:65], v[188:195], v[236:243], v[62:65]
	v_mfma_f32_16x16x128_f8f6f4 v[58:61], v[204:211], v[236:243], v[58:61]
	s_setprio 0
	s_barrier
	s_mov_b32 m0, s80
	v_lshl_add_u64 v[196:197], v[150:151], 0, s[30:31]
	s_add_u32 s82, s72, 0x8300
	ds_read_b128 v[212:215], v161 offset:16384
	ds_read_b128 v[216:219], v161 offset:17408
	ds_read_b128 v[220:223], v161 offset:18432
	ds_read_b128 v[224:227], v161 offset:19456
	ds_read_b128 v[228:231], v161 offset:20480
	ds_read_b128 v[232:235], v161 offset:21504
	ds_read_b128 v[236:239], v161 offset:22528
	ds_read_b128 v[240:243], v161 offset:23552
	global_load_lds_dwordx4 v[196:197], off
	v_lshl_add_u64 v[196:197], v[152:153], 0, s[30:31]
	s_mov_b32 m0, s76
	s_addc_u32 s83, s73, 0
	global_load_lds_dwordx4 v[196:197], off
	v_lshl_add_u64 v[196:197], s[82:83], 0, v[140:141]
	s_mov_b32 m0, s77
	s_nop 0
	global_load_lds_dwordx4 v[196:197], off
	v_lshl_add_u64 v[196:197], s[82:83], 0, v[144:145]
	s_mov_b32 m0, s78
	s_nop 0
	global_load_lds_dwordx4 v[196:197], off
	v_lshl_add_u64 v[196:197], v[154:155], 0, s[30:31]
	s_mov_b32 m0, s49
	s_nop 0
	global_load_lds_dwordx4 v[196:197], off
	v_lshl_add_u64 v[196:197], v[156:157], 0, s[30:31]
	s_mov_b32 m0, s51
	s_nop 0
	global_load_lds_dwordx4 v[196:197], off
	s_waitcnt vmcnt(8)
	s_waitcnt lgkmcnt(0)
	s_barrier
	s_setprio 1
	s_waitcnt lgkmcnt(0)
	v_mfma_f32_16x16x128_f8f6f4 v[86:89], v[172:179], v[212:219], v[86:89]
	v_mfma_f32_16x16x128_f8f6f4 v[82:85], v[180:187], v[212:219], v[82:85]
	v_mfma_f32_16x16x128_f8f6f4 v[54:57], v[172:179], v[220:227], v[54:57]
	v_mfma_f32_16x16x128_f8f6f4 v[50:53], v[180:187], v[220:227], v[50:53]
	v_mfma_f32_16x16x128_f8f6f4 v[38:41], v[172:179], v[228:235], v[38:41]
	v_mfma_f32_16x16x128_f8f6f4 v[34:37], v[180:187], v[228:235], v[34:37]
	v_mfma_f32_16x16x128_f8f6f4 v[22:25], v[172:179], v[236:243], v[22:25]
	v_mfma_f32_16x16x128_f8f6f4 v[18:21], v[180:187], v[236:243], v[18:21]
	s_setprio 0
	s_setprio 1
	v_mfma_f32_16x16x128_f8f6f4 v[70:73], v[188:195], v[212:219], v[70:73]
	v_mfma_f32_16x16x128_f8f6f4 v[66:69], v[204:211], v[212:219], v[66:69]
	v_mfma_f32_16x16x128_f8f6f4 v[46:49], v[188:195], v[220:227], v[46:49]
	v_mfma_f32_16x16x128_f8f6f4 v[42:45], v[204:211], v[220:227], v[42:45]
	v_mfma_f32_16x16x128_f8f6f4 v[30:33], v[188:195], v[228:235], v[30:33]
	v_mfma_f32_16x16x128_f8f6f4 v[26:29], v[204:211], v[228:235], v[26:29]
	v_mfma_f32_16x16x128_f8f6f4 v[14:17], v[188:195], v[236:243], v[14:17]
	v_mfma_f32_16x16x128_f8f6f4 v[10:13], v[204:211], v[236:243], v[10:13]
	s_setprio 0
	s_barrier
	ds_read_b128 v[172:175], v158
	ds_read_b128 v[176:179], v158 offset:1024
	ds_read_b128 v[180:183], v158 offset:2048
	ds_read_b128 v[184:187], v158 offset:3072
	ds_read_b128 v[188:191], v159
	ds_read_b128 v[192:195], v159 offset:1024
	ds_read_b128 v[204:207], v159 offset:2048
	ds_read_b128 v[208:211], v159 offset:3072
	s_add_u32 s82, s68, 0x20300
	s_addc_u32 s83, s69, 0
	s_mov_b32 m0, s59
	v_lshl_add_u64 v[196:197], s[82:83], 0, v[138:139]
	ds_read_b128 v[212:215], v161 offset:32768
	ds_read_b128 v[216:219], v161 offset:33792
	ds_read_b128 v[220:223], v161 offset:34816
	ds_read_b128 v[224:227], v161 offset:35840
	ds_read_b128 v[228:231], v161 offset:36864
	ds_read_b128 v[232:235], v161 offset:37888
	ds_read_b128 v[236:239], v161 offset:38912
	ds_read_b128 v[240:243], v161 offset:39936
	global_load_lds_dwordx4 v[196:197], off
	v_lshl_add_u64 v[196:197], s[82:83], 0, v[142:143]
	s_mov_b32 m0, s60
	s_nop 0
	global_load_lds_dwordx4 v[196:197], off
	s_waitcnt vmcnt(8)
	s_waitcnt lgkmcnt(0)
	s_barrier
	s_setprio 1
	s_waitcnt lgkmcnt(0)
	v_mfma_f32_16x16x128_f8f6f4 v[134:137], v[172:179], v[212:219], v[134:137]
	v_mfma_f32_16x16x128_f8f6f4 v[130:133], v[180:187], v[212:219], v[130:133]
	v_mfma_f32_16x16x128_f8f6f4 v[118:121], v[172:179], v[220:227], v[118:121]
	v_mfma_f32_16x16x128_f8f6f4 v[114:117], v[180:187], v[220:227], v[114:117]
	v_mfma_f32_16x16x128_f8f6f4 v[102:105], v[172:179], v[228:235], v[102:105]
	v_mfma_f32_16x16x128_f8f6f4 v[98:101], v[180:187], v[228:235], v[98:101]
	v_mfma_f32_16x16x128_f8f6f4 v[78:81], v[172:179], v[236:243], v[78:81]
	v_mfma_f32_16x16x128_f8f6f4 v[74:77], v[180:187], v[236:243], v[74:77]
	s_setprio 0
	s_setprio 1
	v_mfma_f32_16x16x128_f8f6f4 v[126:129], v[188:195], v[212:219], v[126:129]
	v_mfma_f32_16x16x128_f8f6f4 v[122:125], v[204:211], v[212:219], v[122:125]
	v_mfma_f32_16x16x128_f8f6f4 v[110:113], v[188:195], v[220:227], v[110:113]
	v_mfma_f32_16x16x128_f8f6f4 v[106:109], v[204:211], v[220:227], v[106:109]
	v_mfma_f32_16x16x128_f8f6f4 v[94:97], v[188:195], v[228:235], v[94:97]
	v_mfma_f32_16x16x128_f8f6f4 v[90:93], v[204:211], v[228:235], v[90:93]
	v_mfma_f32_16x16x128_f8f6f4 v[62:65], v[188:195], v[236:243], v[62:65]
	v_mfma_f32_16x16x128_f8f6f4 v[58:61], v[204:211], v[236:243], v[58:61]
	s_setprio 0
	s_barrier
	s_mov_b32 m0, s79
	v_lshl_add_u64 v[150:151], v[150:151], 0, s[34:35]
	s_add_u32 s72, s72, 0x8380
	ds_read_b128 v[212:215], v161 offset:49152
	ds_read_b128 v[216:219], v161 offset:50176
	ds_read_b128 v[220:223], v161 offset:51200
	ds_read_b128 v[224:227], v161 offset:52224
	ds_read_b128 v[228:231], v161 offset:53248
	ds_read_b128 v[232:235], v161 offset:54272
	ds_read_b128 v[236:239], v161 offset:55296
	ds_read_b128 v[240:243], v161 offset:56320
	global_load_lds_dwordx4 v[150:151], off
	v_lshl_add_u64 v[150:151], v[152:153], 0, s[34:35]
	s_mov_b32 m0, s39
	s_addc_u32 s73, s73, 0
	global_load_lds_dwordx4 v[150:151], off
	v_lshl_add_u64 v[150:151], s[72:73], 0, v[140:141]
	s_mov_b32 m0, s41
	s_nop 0
	global_load_lds_dwordx4 v[150:151], off
	v_lshl_add_u64 v[150:151], s[72:73], 0, v[144:145]
	s_mov_b32 m0, s71
	s_nop 0
	global_load_lds_dwordx4 v[150:151], off
	v_lshl_add_u64 v[150:151], v[154:155], 0, s[34:35]
	s_mov_b32 m0, s61
	s_nop 0
	global_load_lds_dwordx4 v[150:151], off
	v_lshl_add_u64 v[150:151], v[156:157], 0, s[34:35]
	s_mov_b32 m0, s62
	s_nop 0
	global_load_lds_dwordx4 v[150:151], off
	s_waitcnt vmcnt(8)
	s_waitcnt lgkmcnt(0)
	s_barrier
	s_setprio 1
	s_waitcnt lgkmcnt(0)
	v_mfma_f32_16x16x128_f8f6f4 v[86:89], v[172:179], v[212:219], v[86:89]
	v_mfma_f32_16x16x128_f8f6f4 v[82:85], v[180:187], v[212:219], v[82:85]
	v_mfma_f32_16x16x128_f8f6f4 v[54:57], v[172:179], v[220:227], v[54:57]
	v_mfma_f32_16x16x128_f8f6f4 v[50:53], v[180:187], v[220:227], v[50:53]
	v_mfma_f32_16x16x128_f8f6f4 v[38:41], v[172:179], v[228:235], v[38:41]
	v_mfma_f32_16x16x128_f8f6f4 v[34:37], v[180:187], v[228:235], v[34:37]
	v_mfma_f32_16x16x128_f8f6f4 v[22:25], v[172:179], v[236:243], v[22:25]
	v_mfma_f32_16x16x128_f8f6f4 v[18:21], v[180:187], v[236:243], v[18:21]
	s_setprio 0
	s_setprio 1
	v_mfma_f32_16x16x128_f8f6f4 v[70:73], v[188:195], v[212:219], v[70:73]
	v_mfma_f32_16x16x128_f8f6f4 v[66:69], v[204:211], v[212:219], v[66:69]
	v_mfma_f32_16x16x128_f8f6f4 v[46:49], v[188:195], v[220:227], v[46:49]
	v_mfma_f32_16x16x128_f8f6f4 v[42:45], v[204:211], v[220:227], v[42:45]
	v_mfma_f32_16x16x128_f8f6f4 v[30:33], v[188:195], v[228:235], v[30:33]
	v_mfma_f32_16x16x128_f8f6f4 v[26:29], v[204:211], v[228:235], v[26:29]
	v_mfma_f32_16x16x128_f8f6f4 v[14:17], v[188:195], v[236:243], v[14:17]
	v_mfma_f32_16x16x128_f8f6f4 v[10:13], v[204:211], v[236:243], v[10:13]
	s_setprio 0
	s_barrier
	ds_read_b128 v[150:153], v162
	ds_read_b128 v[154:157], v162 offset:1024
	ds_read_b128 v[172:175], v162 offset:2048
	ds_read_b128 v[176:179], v162 offset:3072
	ds_read_b128 v[180:183], v163
	ds_read_b128 v[184:187], v163 offset:1024
	ds_read_b128 v[188:191], v163 offset:2048
	ds_read_b128 v[192:195], v163 offset:3072
	s_add_u32 s68, s68, 0x20380
	s_addc_u32 s69, s69, 0
	s_mov_b32 m0, s63
	v_lshl_add_u64 v[196:197], s[68:69], 0, v[138:139]
	ds_read_b128 v[204:207], v161
	ds_read_b128 v[208:211], v161 offset:1024
	ds_read_b128 v[212:215], v161 offset:2048
	ds_read_b128 v[216:219], v161 offset:3072
	ds_read_b128 v[220:223], v161 offset:4096
	ds_read_b128 v[224:227], v161 offset:5120
	ds_read_b128 v[228:231], v161 offset:6144
	ds_read_b128 v[232:235], v161 offset:7168
	global_load_lds_dwordx4 v[196:197], off
	v_lshl_add_u64 v[196:197], s[68:69], 0, v[142:143]
	s_mov_b32 m0, s64
	s_nop 0
	global_load_lds_dwordx4 v[196:197], off
	s_waitcnt vmcnt(8)
	s_waitcnt lgkmcnt(0)
	s_barrier
	s_setprio 1
	s_waitcnt lgkmcnt(0)
	v_mfma_f32_16x16x128_f8f6f4 v[134:137], v[150:157], v[204:211], v[134:137]
	v_mfma_f32_16x16x128_f8f6f4 v[130:133], v[172:179], v[204:211], v[130:133]
	v_mfma_f32_16x16x128_f8f6f4 v[118:121], v[150:157], v[212:219], v[118:121]
	v_mfma_f32_16x16x128_f8f6f4 v[114:117], v[172:179], v[212:219], v[114:117]
	v_mfma_f32_16x16x128_f8f6f4 v[102:105], v[150:157], v[220:227], v[102:105]
	v_mfma_f32_16x16x128_f8f6f4 v[98:101], v[172:179], v[220:227], v[98:101]
	v_mfma_f32_16x16x128_f8f6f4 v[78:81], v[150:157], v[228:235], v[78:81]
	v_mfma_f32_16x16x128_f8f6f4 v[74:77], v[172:179], v[228:235], v[74:77]
	s_setprio 0
	s_setprio 1
	v_mfma_f32_16x16x128_f8f6f4 v[126:129], v[180:187], v[204:211], v[126:129]
	v_mfma_f32_16x16x128_f8f6f4 v[122:125], v[188:195], v[204:211], v[122:125]
	v_mfma_f32_16x16x128_f8f6f4 v[110:113], v[180:187], v[212:219], v[110:113]
	v_mfma_f32_16x16x128_f8f6f4 v[106:109], v[188:195], v[212:219], v[106:109]
	v_mfma_f32_16x16x128_f8f6f4 v[94:97], v[180:187], v[220:227], v[94:97]
	v_mfma_f32_16x16x128_f8f6f4 v[90:93], v[188:195], v[220:227], v[90:93]
	v_mfma_f32_16x16x128_f8f6f4 v[62:65], v[180:187], v[228:235], v[62:65]
	v_mfma_f32_16x16x128_f8f6f4 v[58:61], v[188:195], v[228:235], v[58:61]
	s_setprio 0
	s_barrier
	s_mov_b32 m0, s80
	v_lshl_add_u64 v[196:197], s[8:9], 0, v[140:141]
	s_add_u32 s68, s8, 0x8000
	ds_read_b128 v[204:207], v161 offset:16384
	ds_read_b128 v[208:211], v161 offset:17408
	ds_read_b128 v[212:215], v161 offset:18432
	ds_read_b128 v[216:219], v161 offset:19456
	ds_read_b128 v[220:223], v161 offset:20480
	ds_read_b128 v[224:227], v161 offset:21504
	ds_read_b128 v[228:231], v161 offset:22528
	ds_read_b128 v[232:235], v161 offset:23552
	global_load_lds_dwordx4 v[196:197], off
	v_lshl_add_u64 v[198:199], s[8:9], 0, v[144:145]
	s_mov_b32 m0, s76
	s_addc_u32 s69, s9, 0
	global_load_lds_dwordx4 v[198:199], off
	v_lshl_add_u64 v[200:201], s[68:69], 0, v[140:141]
	s_mov_b32 m0, s77
	v_lshl_add_u64 v[236:237], s[74:75], 0, v[142:143]
	global_load_lds_dwordx4 v[200:201], off
	v_lshl_add_u64 v[200:201], s[68:69], 0, v[144:145]
	s_mov_b32 m0, s78
	s_nop 0
	global_load_lds_dwordx4 v[200:201], off
	v_lshl_add_u64 v[200:201], s[74:75], 0, v[138:139]
	s_mov_b32 m0, s49
	s_nop 0
	global_load_lds_dwordx4 v[200:201], off
	s_mov_b32 m0, s51
	s_nop 0
	global_load_lds_dwordx4 v[236:237], off
	s_waitcnt vmcnt(8)
	s_waitcnt lgkmcnt(0)
	s_barrier
	s_setprio 1
	s_waitcnt lgkmcnt(0)
	v_mfma_f32_16x16x128_f8f6f4 v[86:89], v[150:157], v[204:211], v[86:89]
	v_mfma_f32_16x16x128_f8f6f4 v[82:85], v[172:179], v[204:211], v[82:85]
	v_mfma_f32_16x16x128_f8f6f4 v[54:57], v[150:157], v[212:219], v[54:57]
	v_mfma_f32_16x16x128_f8f6f4 v[50:53], v[172:179], v[212:219], v[50:53]
	v_mfma_f32_16x16x128_f8f6f4 v[38:41], v[150:157], v[220:227], v[38:41]
	v_mfma_f32_16x16x128_f8f6f4 v[34:37], v[172:179], v[220:227], v[34:37]
	v_mfma_f32_16x16x128_f8f6f4 v[22:25], v[150:157], v[228:235], v[22:25]
	v_mfma_f32_16x16x128_f8f6f4 v[18:21], v[172:179], v[228:235], v[18:21]
	s_setprio 0
	s_setprio 1
	v_mfma_f32_16x16x128_f8f6f4 v[70:73], v[180:187], v[204:211], v[70:73]
	v_mfma_f32_16x16x128_f8f6f4 v[66:69], v[188:195], v[204:211], v[66:69]
	v_mfma_f32_16x16x128_f8f6f4 v[46:49], v[180:187], v[212:219], v[46:49]
	v_mfma_f32_16x16x128_f8f6f4 v[42:45], v[188:195], v[212:219], v[42:45]
	v_mfma_f32_16x16x128_f8f6f4 v[30:33], v[180:187], v[220:227], v[30:33]
	v_mfma_f32_16x16x128_f8f6f4 v[26:29], v[188:195], v[220:227], v[26:29]
	v_mfma_f32_16x16x128_f8f6f4 v[14:17], v[180:187], v[228:235], v[14:17]
	v_mfma_f32_16x16x128_f8f6f4 v[10:13], v[188:195], v[228:235], v[10:13]
	s_setprio 0
	s_barrier
	ds_read_b128 v[150:153], v158
	ds_read_b128 v[154:157], v158 offset:1024
	ds_read_b128 v[172:175], v158 offset:2048
	ds_read_b128 v[176:179], v158 offset:3072
	ds_read_b128 v[180:183], v159
	ds_read_b128 v[184:187], v159 offset:1024
	ds_read_b128 v[188:191], v159 offset:2048
	ds_read_b128 v[192:195], v159 offset:3072
	s_add_u32 s68, s74, 0x20000
	s_addc_u32 s69, s75, 0
	s_mov_b32 m0, s59
	v_lshl_add_u64 v[158:159], s[68:69], 0, v[138:139]
	ds_read_b128 v[204:207], v161 offset:32768
	ds_read_b128 v[208:211], v161 offset:33792
	ds_read_b128 v[212:215], v161 offset:34816
	ds_read_b128 v[216:219], v161 offset:35840
	ds_read_b128 v[220:223], v161 offset:36864
	ds_read_b128 v[224:227], v161 offset:37888
	ds_read_b128 v[228:231], v161 offset:38912
	ds_read_b128 v[232:235], v161 offset:39936
	global_load_lds_dwordx4 v[158:159], off
	v_lshl_add_u64 v[158:159], s[68:69], 0, v[142:143]
	s_mov_b32 m0, s60
	s_nop 0
	global_load_lds_dwordx4 v[158:159], off
	s_waitcnt vmcnt(8)
	s_waitcnt lgkmcnt(0)
	s_barrier
	s_setprio 1
	s_waitcnt lgkmcnt(0)
	v_mfma_f32_16x16x128_f8f6f4 v[134:137], v[150:157], v[204:211], v[134:137]
	v_mfma_f32_16x16x128_f8f6f4 v[130:133], v[172:179], v[204:211], v[130:133]
	v_mfma_f32_16x16x128_f8f6f4 v[118:121], v[150:157], v[212:219], v[118:121]
	v_mfma_f32_16x16x128_f8f6f4 v[114:117], v[172:179], v[212:219], v[114:117]
	v_mfma_f32_16x16x128_f8f6f4 v[102:105], v[150:157], v[220:227], v[102:105]
	v_mfma_f32_16x16x128_f8f6f4 v[98:101], v[172:179], v[220:227], v[98:101]
	v_mfma_f32_16x16x128_f8f6f4 v[78:81], v[150:157], v[228:235], v[78:81]
	v_mfma_f32_16x16x128_f8f6f4 v[74:77], v[172:179], v[228:235], v[74:77]
	s_setprio 0
	s_setprio 1
	v_mfma_f32_16x16x128_f8f6f4 v[126:129], v[180:187], v[204:211], v[126:129]
	v_mfma_f32_16x16x128_f8f6f4 v[122:125], v[188:195], v[204:211], v[122:125]
	v_mfma_f32_16x16x128_f8f6f4 v[110:113], v[180:187], v[212:219], v[110:113]
	v_mfma_f32_16x16x128_f8f6f4 v[106:109], v[188:195], v[212:219], v[106:109]
	v_mfma_f32_16x16x128_f8f6f4 v[94:97], v[180:187], v[220:227], v[94:97]
	v_mfma_f32_16x16x128_f8f6f4 v[90:93], v[188:195], v[220:227], v[90:93]
	v_mfma_f32_16x16x128_f8f6f4 v[62:65], v[180:187], v[228:235], v[62:65]
	v_mfma_f32_16x16x128_f8f6f4 v[58:61], v[188:195], v[228:235], v[58:61]
	s_setprio 0
	s_barrier
	s_mov_b32 m0, s79
	v_lshl_add_u64 v[158:159], v[196:197], 0, s[18:19]
	s_add_u32 s8, s8, 0x8080
	ds_read_b128 v[204:207], v161 offset:49152
	ds_read_b128 v[208:211], v161 offset:50176
	ds_read_b128 v[212:215], v161 offset:51200
	ds_read_b128 v[216:219], v161 offset:52224
	ds_read_b128 v[220:223], v161 offset:53248
	ds_read_b128 v[224:227], v161 offset:54272
	ds_read_b128 v[228:231], v161 offset:55296
	ds_read_b128 v[232:235], v161 offset:56320
	global_load_lds_dwordx4 v[158:159], off
	v_lshl_add_u64 v[158:159], v[198:199], 0, s[18:19]
	s_mov_b32 m0, s39
	s_addc_u32 s9, s9, 0
	global_load_lds_dwordx4 v[158:159], off
	v_lshl_add_u64 v[158:159], s[8:9], 0, v[140:141]
	s_mov_b32 m0, s41
	s_nop 0
	global_load_lds_dwordx4 v[158:159], off
	v_lshl_add_u64 v[158:159], s[8:9], 0, v[144:145]
	s_mov_b32 m0, s71
	s_nop 0
	global_load_lds_dwordx4 v[158:159], off
	v_lshl_add_u64 v[158:159], v[200:201], 0, s[18:19]
	s_mov_b32 m0, s61
	s_nop 0
	global_load_lds_dwordx4 v[158:159], off
	v_lshl_add_u64 v[158:159], v[236:237], 0, s[18:19]
	s_mov_b32 m0, s62
	s_nop 0
	global_load_lds_dwordx4 v[158:159], off
	s_waitcnt vmcnt(8)
	s_waitcnt lgkmcnt(0)
	s_barrier
	s_setprio 1
	s_waitcnt lgkmcnt(0)
	v_mfma_f32_16x16x128_f8f6f4 v[86:89], v[150:157], v[204:211], v[86:89]
	v_mfma_f32_16x16x128_f8f6f4 v[82:85], v[172:179], v[204:211], v[82:85]
	v_mfma_f32_16x16x128_f8f6f4 v[54:57], v[150:157], v[212:219], v[54:57]
	v_mfma_f32_16x16x128_f8f6f4 v[50:53], v[172:179], v[212:219], v[50:53]
	v_mfma_f32_16x16x128_f8f6f4 v[38:41], v[150:157], v[220:227], v[38:41]
	v_mfma_f32_16x16x128_f8f6f4 v[34:37], v[172:179], v[220:227], v[34:37]
	v_mfma_f32_16x16x128_f8f6f4 v[22:25], v[150:157], v[228:235], v[22:25]
	v_mfma_f32_16x16x128_f8f6f4 v[18:21], v[172:179], v[228:235], v[18:21]
	s_setprio 0
	s_setprio 1
	v_mfma_f32_16x16x128_f8f6f4 v[70:73], v[180:187], v[204:211], v[70:73]
	v_mfma_f32_16x16x128_f8f6f4 v[66:69], v[188:195], v[204:211], v[66:69]
	v_mfma_f32_16x16x128_f8f6f4 v[46:49], v[180:187], v[212:219], v[46:49]
	v_mfma_f32_16x16x128_f8f6f4 v[42:45], v[188:195], v[212:219], v[42:45]
	v_mfma_f32_16x16x128_f8f6f4 v[30:33], v[180:187], v[220:227], v[30:33]
	v_mfma_f32_16x16x128_f8f6f4 v[26:29], v[188:195], v[220:227], v[26:29]
	v_mfma_f32_16x16x128_f8f6f4 v[14:17], v[180:187], v[228:235], v[14:17]
	v_mfma_f32_16x16x128_f8f6f4 v[10:13], v[188:195], v[228:235], v[10:13]
	s_setprio 0
	s_barrier
	v_cndmask_b32_e64 v150, 0, 1, s[6:7]
	v_cmp_ne_u32_e64 s[8:9], 1, v150
	s_andn2_b64 vcc, exec, s[6:7]
	s_cbranch_vccnz .LBB0_1625
	s_add_u32 s6, s44, 0x20080
	s_addc_u32 s7, s45, 0
	s_mov_b32 m0, s63
	v_lshl_add_u64 v[150:151], s[6:7], 0, v[138:139]
	v_lshl_add_u64 v[152:153], s[6:7], 0, v[142:143]
	global_load_lds_dwordx4 v[150:151], off
	s_mov_b32 m0, s64
	s_nop 0
	global_load_lds_dwordx4 v[152:153], off

.LBB0_1627:
	s_cmp_lg_u64 s[8:9], 0
	s_cbranch_scc1 .Ldpf_skip_0
	v_lshrrev_b32_e32 v244, 1, v0
	v_and_b32_e32 v245, 1, v0
	v_lshlrev_b32_e32 v244, 10, v244
	v_lshl_add_u32 v244, v245, 7, v244
	s_add_u32 s92, s44, 0x100
	s_addc_u32 s93, s45, 0
	global_load_dword v246, v244, s[92:93]
	global_load_dword v247, v244, s[92:93] offset:256
	global_load_dword v248, v244, s[92:93] offset:512
.Ldpf_skip_0:
	v_lshlrev_b32_e32 v158, 16, v6
	v_and_b32_e32 v159, 0xffff0000, v6
	v_lshlrev_b32_e32 v154, 16, v8
	v_and_b32_e32 v155, 0xffff0000, v8
	v_lshlrev_b32_e32 v156, 16, v7
	v_and_b32_e32 v157, 0xffff0000, v7
	v_lshlrev_b32_e32 v152, 16, v9
	v_and_b32_e32 v153, 0xffff0000, v9
	s_waitcnt vmcnt(13)
	v_lshlrev_b32_e32 v6, 16, v4
	v_and_b32_e32 v7, 0xffff0000, v4
	v_mul_f32_e32 v4, 0x41000000, v146
	v_pk_fma_f32 v[134:135], v[134:135], s[36:37], v[158:159] op_sel_hi:[1,0,1]
	v_pk_fma_f32 v[130:131], v[130:131], s[36:37], v[154:155] op_sel_hi:[1,0,1]
	v_pk_fma_f32 v[136:137], v[136:137], s[36:37], v[156:157] op_sel_hi:[1,0,1]
	v_pk_mul_f32 v[134:135], v[4:5], v[134:135] op_sel_hi:[0,1]
	v_pk_fma_f32 v[132:133], v[132:133], s[36:37], v[152:153] op_sel_hi:[1,0,1]
	v_pk_mul_f32 v[130:131], v[4:5], v[130:131] op_sel_hi:[0,1]
	v_lshlrev_b32_e32 v150, 16, v2
	v_and_b32_e32 v151, 0xffff0000, v2
	v_lshlrev_b32_e32 v8, 16, v3
	v_and_b32_e32 v9, 0xffff0000, v3
	v_lshlrev_b32_e32 v2, 16, v5
	v_and_b32_e32 v3, 0xffff0000, v5
	v_pk_mul_f32 v[136:137], v[4:5], v[136:137] op_sel_hi:[0,1]
	v_pk_mul_f32 v[132:133], v[4:5], v[132:133] op_sel_hi:[0,1]
	v_med3_f32 v5, v134, s70, v164
	v_med3_f32 v134, v130, s70, v164
	v_med3_f32 v135, v135, s70, v164
	v_mov_b32_e32 v130, 0
	v_cvt_pk_fp8_f32 v130, v5, v135
	v_med3_f32 v136, v136, s70, v164
	v_med3_f32 v5, v137, s70, v164
	v_pk_fma_f32 v[126:127], v[126:127], s[36:37], v[150:151] op_sel_hi:[1,0,1]
	v_pk_fma_f32 v[128:129], v[128:129], s[36:37], v[8:9] op_sel_hi:[1,0,1]
	v_pk_fma_f32 v[122:123], v[122:123], s[36:37], v[6:7] op_sel_hi:[1,0,1]
	v_pk_fma_f32 v[124:125], v[124:125], s[36:37], v[2:3] op_sel_hi:[1,0,1]
	v_cvt_pk_fp8_f32 v130, v136, v5 op_sel:[0,0,1]
	v_pk_mul_f32 v[128:129], v[4:5], v[128:129] op_sel_hi:[0,1]
	v_pk_mul_f32 v[126:127], v[4:5], v[126:127] op_sel_hi:[0,1]
	v_pk_mul_f32 v[124:125], v[4:5], v[124:125] op_sel_hi:[0,1]
	v_pk_mul_f32 v[4:5], v[4:5], v[122:123] op_sel_hi:[0,1]
	v_med3_f32 v146, v131, s70, v164
	v_mov_b32_e32 v131, 0
	v_med3_f32 v122, v126, s70, v164
	v_med3_f32 v123, v4, s70, v164
	v_med3_f32 v126, v127, s70, v164
	v_med3_f32 v127, v5, s70, v164
	v_mov_b32_e32 v4, 0
	v_mov_b32_e32 v5, 0
	v_cvt_pk_fp8_f32 v131, v134, v146
	v_cvt_pk_fp8_f32 v4, v122, v126
	v_cvt_pk_fp8_f32 v5, v123, v127
	v_mov_b32_e32 v171, v0
	v_med3_f32 v132, v132, s70, v164
	v_readfirstlane_b32 s39, v171
	s_lshr_b32 s6, s39, 6
	v_med3_f32 v133, v133, s70, v164
	v_med3_f32 v128, v128, s70, v164
	v_med3_f32 v124, v124, s70, v164
	v_med3_f32 v122, v129, s70, v164
	v_med3_f32 v123, v125, s70, v164
	s_mulk_i32 s6, 0xb00
	v_cvt_pk_fp8_f32 v131, v132, v133 op_sel:[0,0,1]
	v_cvt_pk_fp8_f32 v4, v128, v122 op_sel:[0,0,1]
	v_cvt_pk_fp8_f32 v5, v124, v123 op_sel:[0,0,1]
	s_add_i32 s6, s6, 0
	v_and_b32_e32 v172, 15, v171
	v_lshrrev_b32_e32 v123, 1, v171
	s_add_i32 s41, s6, 0x20000
	v_mul_u32_u24_e32 v122, 0x50, v172
	v_and_b32_e32 v123, 24, v123
	v_add3_u32 v122, s41, v122, v123
	s_and_b32 s7, s39, 0xc0
	ds_write2_b64 v122, v[130:131], v[4:5] offset1:4
	v_bfe_u32 v4, v171, 2, 4
	s_ashr_i32 s39, s39, 2
	v_mul_u32_u24_e32 v5, 0x50, v4
	v_lshlrev_b32_e32 v123, 4, v171
	s_andn2_b32 s39, s39, 63
	v_lshl_or_b32 v4, s48, 8, v4
	v_and_b32_e32 v146, 48, v123
	v_add_u32_e32 v4, s39, v4
	v_mul_f32_e32 v130, 0x41000000, v170
	v_pk_fma_f32 v[118:119], v[118:119], s[36:37], v[158:159] op_sel_hi:[1,0,1]
	v_pk_fma_f32 v[114:115], v[114:115], s[36:37], v[154:155] op_sel_hi:[1,0,1]
	v_add3_u32 v123, s41, v5, v146
	v_ashrrev_i32_e32 v5, 31, v4
	v_pk_mul_f32 v[118:119], v[130:131], v[118:119] op_sel_hi:[0,1]
	v_pk_mul_f32 v[114:115], v[130:131], v[114:115] op_sel_hi:[0,1]
	v_lshlrev_b64 v[128:129], 10, v[4:5]
	v_med3_f32 v5, v118, s70, v164
	v_med3_f32 v118, v114, s70, v164
	v_med3_f32 v119, v119, s70, v164
	v_mov_b32_e32 v114, v147
	v_cvt_pk_fp8_f32 v114, v5, v119
	v_pk_fma_f32 v[120:121], v[120:121], s[36:37], v[156:157] op_sel_hi:[1,0,1]
	v_pk_fma_f32 v[116:117], v[116:117], s[36:37], v[152:153] op_sel_hi:[1,0,1]
	v_pk_mul_f32 v[120:121], v[130:131], v[120:121] op_sel_hi:[0,1]
	v_pk_mul_f32 v[116:117], v[130:131], v[116:117] op_sel_hi:[0,1]
	v_med3_f32 v131, v115, s70, v164
	v_pk_fma_f32 v[110:111], v[110:111], s[36:37], v[150:151] op_sel_hi:[1,0,1]
	v_pk_fma_f32 v[106:107], v[106:107], s[36:37], v[6:7] op_sel_hi:[1,0,1]
	v_med3_f32 v120, v120, s70, v164
	v_med3_f32 v5, v121, s70, v164
	v_pk_mul_f32 v[110:111], v[130:131], v[110:111] op_sel_hi:[0,1]
	v_pk_mul_f32 v[106:107], v[130:131], v[106:107] op_sel_hi:[0,1]
	v_cvt_pk_fp8_f32 v114, v120, v5 op_sel:[0,0,1]
	v_med3_f32 v5, v110, s70, v164
	v_med3_f32 v110, v106, s70, v164
	v_med3_f32 v111, v111, s70, v164
	v_mov_b32_e32 v106, v147
	v_cvt_pk_fp8_f32 v106, v5, v111
	v_pk_fma_f32 v[112:113], v[112:113], s[36:37], v[8:9] op_sel_hi:[1,0,1]
	v_mov_b32_e32 v115, v147
	v_pk_mul_f32 v[112:113], v[130:131], v[112:113] op_sel_hi:[0,1]
	v_med3_f32 v112, v112, s70, v164
	v_med3_f32 v5, v113, s70, v164
	v_cvt_pk_fp8_f32 v106, v112, v5 op_sel:[0,0,1]
	v_mul_f32_e32 v112, 0x41000000, v169
	v_pk_fma_f32 v[102:103], v[102:103], s[36:37], v[158:159] op_sel_hi:[1,0,1]
	v_pk_fma_f32 v[98:99], v[98:99], s[36:37], v[154:155] op_sel_hi:[1,0,1]
	v_cvt_pk_fp8_f32 v115, v118, v131
	v_pk_mul_f32 v[102:103], v[112:113], v[102:103] op_sel_hi:[0,1]
	v_pk_mul_f32 v[98:99], v[112:113], v[98:99] op_sel_hi:[0,1]
	v_med3_f32 v5, v102, s70, v164
	v_med3_f32 v102, v98, s70, v164
	v_med3_f32 v103, v103, s70, v164
	v_mov_b32_e32 v98, v147
	v_cvt_pk_fp8_f32 v98, v5, v103
	v_med3_f32 v116, v116, s70, v164
	v_med3_f32 v117, v117, s70, v164
	v_pk_fma_f32 v[104:105], v[104:105], s[36:37], v[156:157] op_sel_hi:[1,0,1]
	v_pk_fma_f32 v[100:101], v[100:101], s[36:37], v[152:153] op_sel_hi:[1,0,1]
	v_cvt_pk_fp8_f32 v115, v116, v117 op_sel:[0,0,1]
	v_med3_f32 v116, v107, s70, v164
	v_mov_b32_e32 v107, v147
	v_pk_mul_f32 v[104:105], v[112:113], v[104:105] op_sel_hi:[0,1]
	v_pk_mul_f32 v[100:101], v[112:113], v[100:101] op_sel_hi:[0,1]
	v_med3_f32 v113, v99, s70, v164
	v_pk_fma_f32 v[94:95], v[94:95], s[36:37], v[150:151] op_sel_hi:[1,0,1]
	v_pk_fma_f32 v[90:91], v[90:91], s[36:37], v[6:7] op_sel_hi:[1,0,1]
	v_cvt_pk_fp8_f32 v107, v110, v116
	v_med3_f32 v104, v104, s70, v164
	v_med3_f32 v5, v105, s70, v164
	v_pk_mul_f32 v[94:95], v[112:113], v[94:95] op_sel_hi:[0,1]
	v_pk_mul_f32 v[90:91], v[112:113], v[90:91] op_sel_hi:[0,1]
	v_pk_fma_f32 v[108:109], v[108:109], s[36:37], v[2:3] op_sel_hi:[1,0,1]
	v_mov_b32_e32 v99, v147
	v_cvt_pk_fp8_f32 v98, v104, v5 op_sel:[0,0,1]
	v_med3_f32 v5, v94, s70, v164
	v_med3_f32 v94, v90, s70, v164
	v_med3_f32 v95, v95, s70, v164
	v_mov_b32_e32 v90, v147
	s_lshl_b32 s6, s50, 8
	ds_read_b128 v[124:127], v123
	v_pk_mul_f32 v[108:109], v[130:131], v[108:109] op_sel_hi:[0,1]
	v_cvt_pk_fp8_f32 v99, v102, v113
	v_cvt_pk_fp8_f32 v90, v5, v95
	s_or_b32 s6, s7, s6
	v_med3_f32 v108, v108, s70, v164
	v_med3_f32 v109, v109, s70, v164
	v_pk_fma_f32 v[96:97], v[96:97], s[36:37], v[8:9] op_sel_hi:[1,0,1]
	s_ashr_i32 s7, s6, 31
	v_lshl_add_u64 v[128:129], s[16:17], 0, v[128:129]
	v_cvt_pk_fp8_f32 v107, v108, v109 op_sel:[0,0,1]
	v_pk_mul_f32 v[96:97], v[112:113], v[96:97] op_sel_hi:[0,1]
	v_lshl_add_u64 v[128:129], v[128:129], 0, s[6:7]
	v_med3_f32 v100, v100, s70, v164
	v_med3_f32 v101, v101, s70, v164
	v_med3_f32 v96, v96, s70, v164
	v_med3_f32 v5, v97, s70, v164
	v_lshl_add_u64 v[108:109], v[128:129], 0, v[146:147]
	v_cvt_pk_fp8_f32 v99, v100, v101 op_sel:[0,0,1]
	v_med3_f32 v100, v91, s70, v164
	v_mov_b32_e32 v91, v147
	v_cvt_pk_fp8_f32 v90, v96, v5 op_sel:[0,0,1]
	v_mul_f32_e32 v96, 0x41000000, v168
	v_pk_fma_f32 v[78:79], v[78:79], s[36:37], v[158:159] op_sel_hi:[1,0,1]
	v_pk_fma_f32 v[74:75], v[74:75], s[36:37], v[154:155] op_sel_hi:[1,0,1]
	s_waitcnt lgkmcnt(0)
	global_store_dwordx4 v[108:109], v[124:127], off
	v_cvt_pk_fp8_f32 v91, v94, v100
	v_pk_fma_f32 v[80:81], v[80:81], s[36:37], v[156:157] op_sel_hi:[1,0,1]
	v_pk_mul_f32 v[78:79], v[96:97], v[78:79] op_sel_hi:[0,1]
	v_pk_fma_f32 v[76:77], v[76:77], s[36:37], v[152:153] op_sel_hi:[1,0,1]
	v_pk_mul_f32 v[74:75], v[96:97], v[74:75] op_sel_hi:[0,1]
	ds_write2_b64 v122, v[114:115], v[106:107] offset1:4
	v_or_b32_e32 v110, 16, v4
	v_pk_fma_f32 v[92:93], v[92:93], s[36:37], v[2:3] op_sel_hi:[1,0,1]
	v_pk_mul_f32 v[80:81], v[96:97], v[80:81] op_sel_hi:[0,1]
	v_pk_mul_f32 v[76:77], v[96:97], v[76:77] op_sel_hi:[0,1]
	v_med3_f32 v5, v78, s70, v164
	v_med3_f32 v78, v74, s70, v164
	v_med3_f32 v79, v79, s70, v164
	v_med3_f32 v97, v75, s70, v164
	v_mov_b32_e32 v74, v147
	v_mov_b32_e32 v75, v147
	ds_read_b128 v[106:109], v123
	v_ashrrev_i32_e32 v111, 31, v110
	v_pk_mul_f32 v[92:93], v[112:113], v[92:93] op_sel_hi:[0,1]
	v_cvt_pk_fp8_f32 v74, v5, v79
	v_cvt_pk_fp8_f32 v75, v78, v97
	v_lshlrev_b64 v[110:111], 10, v[110:111]
	v_med3_f32 v92, v92, s70, v164
	v_med3_f32 v93, v93, s70, v164
	v_lshl_add_u64 v[110:111], s[16:17], 0, v[110:111]
	v_cvt_pk_fp8_f32 v91, v92, v93 op_sel:[0,0,1]
	v_pk_fma_f32 v[62:63], v[62:63], s[36:37], v[150:151] op_sel_hi:[1,0,1]
	v_pk_fma_f32 v[58:59], v[58:59], s[36:37], v[6:7] op_sel_hi:[1,0,1]
	v_lshl_add_u64 v[110:111], v[110:111], 0, s[6:7]
	v_med3_f32 v80, v80, s70, v164
	v_med3_f32 v76, v76, s70, v164
	v_med3_f32 v5, v81, s70, v164
	v_med3_f32 v77, v77, s70, v164
	v_pk_mul_f32 v[62:63], v[96:97], v[62:63] op_sel_hi:[0,1]
	v_pk_mul_f32 v[58:59], v[96:97], v[58:59] op_sel_hi:[0,1]
	v_lshl_add_u64 v[92:93], v[110:111], 0, v[146:147]
	v_cvt_pk_fp8_f32 v74, v80, v5 op_sel:[0,0,1]
	v_cvt_pk_fp8_f32 v75, v76, v77 op_sel:[0,0,1]
	v_med3_f32 v5, v62, s70, v164
	v_med3_f32 v62, v58, s70, v164
	v_med3_f32 v63, v63, s70, v164
	v_med3_f32 v76, v59, s70, v164
	v_mov_b32_e32 v58, v147
	v_mov_b32_e32 v59, v147
	s_waitcnt lgkmcnt(0)
	global_store_dwordx4 v[92:93], v[106:109], off
	v_cvt_pk_fp8_f32 v58, v5, v63
	v_cvt_pk_fp8_f32 v59, v62, v76
	ds_write2_b64 v122, v[98:99], v[90:91] offset1:4
	v_or_b32_e32 v94, 32, v4
	v_pk_fma_f32 v[64:65], v[64:65], s[36:37], v[8:9] op_sel_hi:[1,0,1]
	v_pk_fma_f32 v[60:61], v[60:61], s[36:37], v[2:3] op_sel_hi:[1,0,1]
	ds_read_b128 v[90:93], v123
	v_ashrrev_i32_e32 v95, 31, v94
	v_pk_mul_f32 v[64:65], v[96:97], v[64:65] op_sel_hi:[0,1]
	v_pk_mul_f32 v[60:61], v[96:97], v[60:61] op_sel_hi:[0,1]
	v_lshlrev_b64 v[94:95], 10, v[94:95]
	v_med3_f32 v64, v64, s70, v164
	v_med3_f32 v60, v60, s70, v164
	v_med3_f32 v5, v65, s70, v164
	v_med3_f32 v61, v61, s70, v164
	v_lshl_add_u64 v[94:95], s[16:17], 0, v[94:95]
	v_cvt_pk_fp8_f32 v58, v64, v5 op_sel:[0,0,1]
	v_cvt_pk_fp8_f32 v59, v60, v61 op_sel:[0,0,1]
	v_lshl_add_u64 v[94:95], v[94:95], 0, s[6:7]
	v_lshl_add_u64 v[60:61], v[94:95], 0, v[146:147]
	s_waitcnt lgkmcnt(0)
	global_store_dwordx4 v[60:61], v[90:93], off
	ds_write2_b64 v122, v[74:75], v[58:59] offset1:4
	v_mul_f32_e32 v64, 0x41000000, v167
	v_pk_fma_f32 v[74:75], v[86:87], s[36:37], v[158:159] op_sel_hi:[1,0,1]
	v_pk_fma_f32 v[78:79], v[82:83], s[36:37], v[154:155] op_sel_hi:[1,0,1]
	v_pk_mul_f32 v[74:75], v[64:65], v[74:75] op_sel_hi:[0,1]
	v_pk_fma_f32 v[76:77], v[88:89], s[36:37], v[156:157] op_sel_hi:[1,0,1]
	v_pk_fma_f32 v[80:81], v[84:85], s[36:37], v[152:153] op_sel_hi:[1,0,1]
	v_pk_mul_f32 v[78:79], v[64:65], v[78:79] op_sel_hi:[0,1]
	v_med3_f32 v5, v74, s70, v164
	v_med3_f32 v75, v75, s70, v164
	v_mov_b32_e32 v74, v147
	v_pk_mul_f32 v[76:77], v[64:65], v[76:77] op_sel_hi:[0,1]
	v_pk_mul_f32 v[80:81], v[64:65], v[80:81] op_sel_hi:[0,1]
	v_med3_f32 v65, v78, s70, v164
	v_med3_f32 v78, v79, s70, v164
	v_cvt_pk_fp8_f32 v74, v5, v75
	v_mov_b32_e32 v75, v147
	v_cvt_pk_fp8_f32 v75, v65, v78
	v_med3_f32 v79, v80, s70, v164
	v_med3_f32 v65, v81, s70, v164
	v_pk_fma_f32 v[70:71], v[70:71], s[36:37], v[150:151] op_sel_hi:[1,0,1]
	v_pk_fma_f32 v[72:73], v[72:73], s[36:37], v[8:9] op_sel_hi:[1,0,1]
	v_pk_fma_f32 v[66:67], v[66:67], s[36:37], v[6:7] op_sel_hi:[1,0,1]
	v_pk_fma_f32 v[68:69], v[68:69], s[36:37], v[2:3] op_sel_hi:[1,0,1]
	v_med3_f32 v76, v76, s70, v164
	v_med3_f32 v5, v77, s70, v164
	v_cvt_pk_fp8_f32 v75, v79, v65 op_sel:[0,0,1]
	v_pk_mul_f32 v[72:73], v[64:65], v[72:73] op_sel_hi:[0,1]
	v_pk_mul_f32 v[70:71], v[64:65], v[70:71] op_sel_hi:[0,1]
	v_pk_mul_f32 v[68:69], v[64:65], v[68:69] op_sel_hi:[0,1]
	v_pk_mul_f32 v[64:65], v[64:65], v[66:67] op_sel_hi:[0,1]
	v_cvt_pk_fp8_f32 v74, v76, v5 op_sel:[0,0,1]
	v_med3_f32 v5, v70, s70, v164
	v_med3_f32 v66, v64, s70, v164
	v_med3_f32 v67, v71, s70, v164
	v_med3_f32 v70, v65, s70, v164
	v_mov_b32_e32 v64, v147
	v_mov_b32_e32 v65, v147
	v_cvt_pk_fp8_f32 v64, v5, v67
	v_cvt_pk_fp8_f32 v65, v66, v70
	v_or_b32_e32 v62, 48, v4
	ds_read_b128 v[58:61], v123
	v_ashrrev_i32_e32 v63, 31, v62
	v_lshlrev_b64 v[62:63], 10, v[62:63]
	v_med3_f32 v71, v72, s70, v164
	v_med3_f32 v68, v68, s70, v164
	v_med3_f32 v5, v73, s70, v164
	v_med3_f32 v66, v69, s70, v164
	v_lshl_add_u64 v[62:63], s[16:17], 0, v[62:63]
	v_cvt_pk_fp8_f32 v64, v71, v5 op_sel:[0,0,1]
	v_cvt_pk_fp8_f32 v65, v68, v66 op_sel:[0,0,1]
	v_lshl_add_u64 v[62:63], v[62:63], 0, s[6:7]
	v_lshl_add_u64 v[62:63], v[62:63], 0, v[146:147]
	s_waitcnt lgkmcnt(0)
	global_store_dwordx4 v[62:63], v[58:61], off
	ds_write2_b64 v122, v[74:75], v[64:65] offset1:4
	v_mul_f32_e32 v64, 0x41000000, v166
	v_pk_fma_f32 v[54:55], v[54:55], s[36:37], v[158:159] op_sel_hi:[1,0,1]
	v_pk_fma_f32 v[50:51], v[50:51], s[36:37], v[154:155] op_sel_hi:[1,0,1]
	v_pk_mul_f32 v[54:55], v[64:65], v[54:55] op_sel_hi:[0,1]
	v_pk_mul_f32 v[50:51], v[64:65], v[50:51] op_sel_hi:[0,1]
	v_med3_f32 v5, v54, s70, v164
	v_med3_f32 v54, v50, s70, v164
	v_med3_f32 v55, v55, s70, v164
	v_mov_b32_e32 v50, v147
	v_cvt_pk_fp8_f32 v50, v5, v55
	v_pk_fma_f32 v[56:57], v[56:57], s[36:37], v[156:157] op_sel_hi:[1,0,1]
	v_pk_fma_f32 v[52:53], v[52:53], s[36:37], v[152:153] op_sel_hi:[1,0,1]
	v_pk_mul_f32 v[56:57], v[64:65], v[56:57] op_sel_hi:[0,1]
	v_pk_mul_f32 v[52:53], v[64:65], v[52:53] op_sel_hi:[0,1]
	v_med3_f32 v65, v51, s70, v164
	v_pk_fma_f32 v[46:47], v[46:47], s[36:37], v[150:151] op_sel_hi:[1,0,1]
	v_pk_fma_f32 v[42:43], v[42:43], s[36:37], v[6:7] op_sel_hi:[1,0,1]
	v_med3_f32 v56, v56, s70, v164
	v_med3_f32 v5, v57, s70, v164
	v_pk_mul_f32 v[46:47], v[64:65], v[46:47] op_sel_hi:[0,1]
	v_pk_mul_f32 v[42:43], v[64:65], v[42:43] op_sel_hi:[0,1]
	v_cvt_pk_fp8_f32 v50, v56, v5 op_sel:[0,0,1]
	v_med3_f32 v5, v46, s70, v164
	v_med3_f32 v46, v42, s70, v164
	v_med3_f32 v47, v47, s70, v164
	v_mov_b32_e32 v42, v147
	v_cvt_pk_fp8_f32 v42, v5, v47
	v_pk_fma_f32 v[48:49], v[48:49], s[36:37], v[8:9] op_sel_hi:[1,0,1]
	v_mov_b32_e32 v51, v147
	v_pk_mul_f32 v[48:49], v[64:65], v[48:49] op_sel_hi:[0,1]
	v_med3_f32 v48, v48, s70, v164
	v_med3_f32 v5, v49, s70, v164
	v_cvt_pk_fp8_f32 v42, v48, v5 op_sel:[0,0,1]
	v_mul_f32_e32 v48, 0x41000000, v165
	v_pk_fma_f32 v[38:39], v[38:39], s[36:37], v[158:159] op_sel_hi:[1,0,1]
	v_pk_fma_f32 v[34:35], v[34:35], s[36:37], v[154:155] op_sel_hi:[1,0,1]
	v_cvt_pk_fp8_f32 v51, v54, v65
	v_pk_mul_f32 v[38:39], v[48:49], v[38:39] op_sel_hi:[0,1]
	v_pk_mul_f32 v[34:35], v[48:49], v[34:35] op_sel_hi:[0,1]
	v_med3_f32 v5, v38, s70, v164
	v_med3_f32 v38, v34, s70, v164
	v_med3_f32 v39, v39, s70, v164
	v_mov_b32_e32 v34, v147
	v_cvt_pk_fp8_f32 v34, v5, v39
	v_med3_f32 v52, v52, s70, v164
	v_med3_f32 v53, v53, s70, v164
	v_pk_fma_f32 v[40:41], v[40:41], s[36:37], v[156:157] op_sel_hi:[1,0,1]
	v_pk_fma_f32 v[36:37], v[36:37], s[36:37], v[152:153] op_sel_hi:[1,0,1]
	v_cvt_pk_fp8_f32 v51, v52, v53 op_sel:[0,0,1]
	v_med3_f32 v52, v43, s70, v164
	v_mov_b32_e32 v43, v147
	v_pk_mul_f32 v[40:41], v[48:49], v[40:41] op_sel_hi:[0,1]
	v_pk_mul_f32 v[36:37], v[48:49], v[36:37] op_sel_hi:[0,1]
	v_med3_f32 v49, v35, s70, v164
	v_pk_fma_f32 v[30:31], v[30:31], s[36:37], v[150:151] op_sel_hi:[1,0,1]
	v_pk_fma_f32 v[26:27], v[26:27], s[36:37], v[6:7] op_sel_hi:[1,0,1]
	v_cvt_pk_fp8_f32 v43, v46, v52
	v_med3_f32 v40, v40, s70, v164
	v_med3_f32 v5, v41, s70, v164
	v_pk_mul_f32 v[30:31], v[48:49], v[30:31] op_sel_hi:[0,1]
	v_pk_mul_f32 v[26:27], v[48:49], v[26:27] op_sel_hi:[0,1]
	v_add_u32_e32 v62, 0x80, v4
	v_pk_fma_f32 v[44:45], v[44:45], s[36:37], v[2:3] op_sel_hi:[1,0,1]
	v_mov_b32_e32 v35, v147
	v_cvt_pk_fp8_f32 v34, v40, v5 op_sel:[0,0,1]
	v_med3_f32 v5, v30, s70, v164
	v_med3_f32 v30, v26, s70, v164
	v_med3_f32 v31, v31, s70, v164
	v_mov_b32_e32 v26, v147
	ds_read_b128 v[58:61], v123
	v_ashrrev_i32_e32 v63, 31, v62
	v_pk_mul_f32 v[44:45], v[64:65], v[44:45] op_sel_hi:[0,1]
	v_cvt_pk_fp8_f32 v35, v38, v49
	v_cvt_pk_fp8_f32 v26, v5, v31
	v_lshlrev_b64 v[62:63], 10, v[62:63]
	v_med3_f32 v44, v44, s70, v164
	v_med3_f32 v45, v45, s70, v164
	v_pk_fma_f32 v[32:33], v[32:33], s[36:37], v[8:9] op_sel_hi:[1,0,1]
	v_lshl_add_u64 v[62:63], s[16:17], 0, v[62:63]
	v_cvt_pk_fp8_f32 v43, v44, v45 op_sel:[0,0,1]
	v_pk_mul_f32 v[32:33], v[48:49], v[32:33] op_sel_hi:[0,1]
	v_lshl_add_u64 v[62:63], v[62:63], 0, s[6:7]
	v_med3_f32 v36, v36, s70, v164
	v_med3_f32 v37, v37, s70, v164
	v_med3_f32 v32, v32, s70, v164
	v_med3_f32 v5, v33, s70, v164
	v_lshl_add_u64 v[44:45], v[62:63], 0, v[146:147]
	v_cvt_pk_fp8_f32 v35, v36, v37 op_sel:[0,0,1]
	v_med3_f32 v36, v27, s70, v164
	v_mov_b32_e32 v27, v147
	v_cvt_pk_fp8_f32 v26, v32, v5 op_sel:[0,0,1]
	v_mul_f32_e32 v32, 0x41000000, v1
	v_pk_fma_f32 v[22:23], v[22:23], s[36:37], v[158:159] op_sel_hi:[1,0,1]
	v_pk_fma_f32 v[18:19], v[18:19], s[36:37], v[154:155] op_sel_hi:[1,0,1]
	s_waitcnt lgkmcnt(0)
	global_store_dwordx4 v[44:45], v[58:61], off
	v_cvt_pk_fp8_f32 v27, v30, v36
	v_pk_mul_f32 v[22:23], v[32:33], v[22:23] op_sel_hi:[0,1]
	v_pk_mul_f32 v[18:19], v[32:33], v[18:19] op_sel_hi:[0,1]
	ds_write2_b64 v122, v[50:51], v[42:43] offset1:4
	v_add_u32_e32 v46, 0x90, v4
	v_pk_fma_f32 v[28:29], v[28:29], s[36:37], v[2:3] op_sel_hi:[1,0,1]
	v_med3_f32 v1, v22, s70, v164
	v_med3_f32 v5, v18, s70, v164
	v_med3_f32 v22, v23, s70, v164
	v_med3_f32 v23, v19, s70, v164
	v_mov_b32_e32 v18, v147
	v_mov_b32_e32 v19, v147
	ds_read_b128 v[42:45], v123
	v_ashrrev_i32_e32 v47, 31, v46
	v_pk_mul_f32 v[28:29], v[48:49], v[28:29] op_sel_hi:[0,1]
	v_cvt_pk_fp8_f32 v18, v1, v22
	v_cvt_pk_fp8_f32 v19, v5, v23
	v_lshlrev_b64 v[46:47], 10, v[46:47]
	v_med3_f32 v28, v28, s70, v164
	v_med3_f32 v29, v29, s70, v164
	v_pk_fma_f32 v[24:25], v[24:25], s[36:37], v[156:157] op_sel_hi:[1,0,1]
	v_pk_fma_f32 v[20:21], v[20:21], s[36:37], v[152:153] op_sel_hi:[1,0,1]
	v_lshl_add_u64 v[46:47], s[16:17], 0, v[46:47]
	v_cvt_pk_fp8_f32 v27, v28, v29 op_sel:[0,0,1]
	v_pk_mul_f32 v[24:25], v[32:33], v[24:25] op_sel_hi:[0,1]
	v_pk_mul_f32 v[20:21], v[32:33], v[20:21] op_sel_hi:[0,1]
	v_pk_fma_f32 v[14:15], v[14:15], s[36:37], v[150:151] op_sel_hi:[1,0,1]
	v_pk_fma_f32 v[6:7], v[10:11], s[36:37], v[6:7] op_sel_hi:[1,0,1]
	v_lshl_add_u64 v[46:47], v[46:47], 0, s[6:7]
	v_med3_f32 v24, v24, s70, v164
	v_med3_f32 v20, v20, s70, v164
	v_med3_f32 v1, v25, s70, v164
	v_med3_f32 v5, v21, s70, v164
	v_pk_mul_f32 v[14:15], v[32:33], v[14:15] op_sel_hi:[0,1]
	v_pk_mul_f32 v[6:7], v[32:33], v[6:7] op_sel_hi:[0,1]
	v_lshl_add_u64 v[28:29], v[46:47], 0, v[146:147]
	v_cvt_pk_fp8_f32 v18, v24, v1 op_sel:[0,0,1]
	v_cvt_pk_fp8_f32 v19, v20, v5 op_sel:[0,0,1]
	v_med3_f32 v1, v14, s70, v164
	v_med3_f32 v5, v6, s70, v164
	v_med3_f32 v10, v15, s70, v164
	v_med3_f32 v11, v7, s70, v164
	v_mov_b32_e32 v6, v147
	v_mov_b32_e32 v7, v147
	s_waitcnt lgkmcnt(0)
	global_store_dwordx4 v[28:29], v[42:45], off
	v_cvt_pk_fp8_f32 v6, v1, v10
	v_cvt_pk_fp8_f32 v7, v5, v11
	ds_write2_b64 v122, v[34:35], v[26:27] offset1:4
	v_add_u32_e32 v30, 0xa0, v4
	v_pk_fma_f32 v[8:9], v[16:17], s[36:37], v[8:9] op_sel_hi:[1,0,1]
	v_pk_fma_f32 v[2:3], v[12:13], s[36:37], v[2:3] op_sel_hi:[1,0,1]
	ds_read_b128 v[26:29], v123
	v_ashrrev_i32_e32 v31, 31, v30
	v_pk_mul_f32 v[8:9], v[32:33], v[8:9] op_sel_hi:[0,1]
	v_pk_mul_f32 v[2:3], v[32:33], v[2:3] op_sel_hi:[0,1]
	v_lshlrev_b64 v[30:31], 10, v[30:31]
	v_med3_f32 v8, v8, s70, v164
	v_med3_f32 v2, v2, s70, v164
	v_med3_f32 v1, v9, s70, v164
	v_med3_f32 v3, v3, s70, v164
	v_lshl_add_u64 v[30:31], s[16:17], 0, v[30:31]
	v_cvt_pk_fp8_f32 v6, v8, v1 op_sel:[0,0,1]
	v_cvt_pk_fp8_f32 v7, v2, v3 op_sel:[0,0,1]
	v_lshl_add_u64 v[30:31], v[30:31], 0, s[6:7]
	v_lshl_add_u64 v[2:3], v[30:31], 0, v[146:147]
	s_waitcnt lgkmcnt(0)
	global_store_dwordx4 v[2:3], v[26:29], off
	ds_write2_b64 v122, v[18:19], v[6:7] offset1:4
	v_add_u32_e32 v2, 0xb0, v4
	ds_read_b128 v[6:9], v123
	v_ashrrev_i32_e32 v3, 31, v2
	v_lshlrev_b64 v[2:3], 10, v[2:3]
	v_lshl_add_u64 v[2:3], s[16:17], 0, v[2:3]
	v_lshl_add_u64 v[2:3], v[2:3], 0, s[6:7]
	v_lshl_add_u64 v[2:3], v[2:3], 0, v[146:147]
	s_waitcnt lgkmcnt(0)
	global_store_dwordx4 v[2:3], v[6:9], off
	s_and_b64 vcc, exec, s[8:9]
	s_mov_b64 s[6:7], -1
	s_cbranch_vccnz .LBB0_1616
	v_mov_b32_e32 v12, v0
	s_lshl_b32 s7, s40, 8
	v_readfirstlane_b32 s6, v12
	s_and_b32 s8, s6, 0xc0
	s_ashr_i32 s6, s6, 2
	s_andn2_b32 s6, s6, 63
	s_add_i32 s6, s6, s7
	v_and_or_b32 v2, v12, 15, s6
	v_ashrrev_i32_e32 v3, 31, v2
	s_lshl_b64 s[6:7], s[42:43], 11
	v_lshl_add_u64 v[4:5], v[2:3], 2, s[12:13]
	v_add_u32_e32 v6, 0x80, v2
	v_add_u32_e32 v8, 0x90, v2
	v_add_u32_e32 v10, 0xa0, v2
	v_add_u32_e32 v2, 0xb0, v2
	s_add_u32 s9, s56, s6
	v_ashrrev_i32_e32 v7, 31, v6
	v_ashrrev_i32_e32 v9, 31, v8
	v_ashrrev_i32_e32 v11, 31, v10
	v_ashrrev_i32_e32 v3, 31, v2
	s_addc_u32 s39, s57, s7
	s_lshl_b32 s6, s38, 8
	v_lshl_add_u64 v[6:7], v[6:7], 2, s[12:13]
	v_lshl_add_u64 v[8:9], v[8:9], 2, s[12:13]
	v_lshl_add_u64 v[10:11], v[10:11], 2, s[12:13]
	v_lshl_add_u64 v[2:3], v[2:3], 2, s[12:13]
	global_load_dword v146, v[4:5], off
	global_load_dword v170, v[4:5], off offset:64
	global_load_dword v169, v[4:5], off offset:128
	global_load_dword v168, v[4:5], off offset:192
	global_load_dword v167, v[6:7], off
	global_load_dword v166, v[8:9], off
	global_load_dword v165, v[10:11], off
	global_load_dword v1, v[2:3], off
	s_ashr_i32 s7, s6, 31
	s_lshl_b64 s[6:7], s[6:7], 1
	s_add_u32 s6, s9, s6
	s_addc_u32 s7, s39, s7
	s_lshl_b32 s8, s8, 1
	s_add_u32 s6, s6, s8
	s_addc_u32 s7, s7, 0
	v_and_b32_e32 v2, 48, v12
	global_load_dwordx4 v[6:9], v2, s[6:7]
	s_nop 0
	global_load_dwordx4 v[2:5], v2, s[6:7] offset:64
	s_andn2_b64 vcc, exec, s[14:15]
	s_cbranch_vccnz .LBB0_1615
	s_barrier
	s_branch .LBB0_1615

.LBB0_3425:
	s_ashr_i32 s43, s42, 31
	s_lshl_b64 s[10:11], s[42:43], 18
	s_add_u32 s46, s6, s10
	ds_read_b128 v[10:13], v162
	ds_read_b128 v[14:17], v162 offset:1024
	ds_read_b128 v[26:29], v162 offset:2048
	ds_read_b128 v[30:33], v162 offset:3072
	ds_read_b128 v[172:175], v163
	ds_read_b128 v[176:179], v163 offset:1024
	ds_read_b128 v[180:183], v163 offset:2048
	ds_read_b128 v[184:187], v163 offset:3072
	s_addc_u32 s47, s7, s11
	s_and_b64 s[10:11], s[8:9], exec
	s_cselect_b32 s71, s47, s65
	s_cselect_b32 s70, s46, s64
	s_ashr_i32 s45, s44, 31
	s_ashr_i32 s41, s40, 31
	s_lshl_b64 s[10:11], s[44:45], 20
	s_lshl_b64 s[48:49], s[40:41], 18
	s_add_u32 s10, s33, s10
	s_addc_u32 s11, s39, s11
	s_add_u32 s48, s10, s48
	s_addc_u32 s49, s11, s49
	s_and_b64 s[10:11], s[8:9], exec
	s_cselect_b32 s11, s49, s67
	s_cselect_b32 s10, s48, s66
	ds_read_b128 v[18:21], v161
	ds_read_b128 v[22:25], v161 offset:1024
	ds_read_b128 v[34:37], v161 offset:2048
	ds_read_b128 v[38:41], v161 offset:3072
	ds_read_b128 v[42:45], v161 offset:4096
	ds_read_b128 v[46:49], v161 offset:5120
	ds_read_b128 v[50:53], v161 offset:6144
	ds_read_b128 v[54:57], v161 offset:7168
	s_waitcnt vmcnt(29)
	s_waitcnt lgkmcnt(0)
	s_barrier
	s_setprio 1
	s_waitcnt lgkmcnt(0)
	v_mfma_f32_16x16x128_f8f6f4 v[134:137], v[10:17], v[18:25], 0
	v_mfma_f32_16x16x128_f8f6f4 v[130:133], v[26:33], v[18:25], 0
	v_mfma_f32_16x16x128_f8f6f4 v[118:121], v[10:17], v[34:41], 0
	v_mfma_f32_16x16x128_f8f6f4 v[114:117], v[26:33], v[34:41], 0
	v_mfma_f32_16x16x128_f8f6f4 v[102:105], v[10:17], v[42:49], 0
	v_mfma_f32_16x16x128_f8f6f4 v[98:101], v[26:33], v[42:49], 0
	v_mfma_f32_16x16x128_f8f6f4 v[78:81], v[10:17], v[50:57], 0
	v_mfma_f32_16x16x128_f8f6f4 v[74:77], v[26:33], v[50:57], 0
	s_setprio 0
	s_setprio 1
	v_mfma_f32_16x16x128_f8f6f4 v[126:129], v[172:179], v[18:25], 0
	v_mfma_f32_16x16x128_f8f6f4 v[122:125], v[180:187], v[18:25], 0
	v_mfma_f32_16x16x128_f8f6f4 v[110:113], v[172:179], v[34:41], 0
	v_mfma_f32_16x16x128_f8f6f4 v[106:109], v[180:187], v[34:41], 0
	v_mfma_f32_16x16x128_f8f6f4 v[94:97], v[172:179], v[42:49], 0
	v_mfma_f32_16x16x128_f8f6f4 v[90:93], v[180:187], v[42:49], 0
	v_mfma_f32_16x16x128_f8f6f4 v[62:65], v[172:179], v[50:57], 0
	v_mfma_f32_16x16x128_f8f6f4 v[58:61], v[180:187], v[50:57], 0
	s_setprio 0
	s_barrier
	s_add_i32 s80, s73, s56
	v_lshl_add_u64 v[150:151], s[66:67], 0, v[140:141]
	s_add_i32 s76, s80, 0x2000
	v_lshl_add_u64 v[18:19], v[150:151], 0, s[24:25]
	s_mov_b32 m0, s80
	v_lshl_add_u64 v[152:153], s[66:67], 0, v[144:145]
	s_add_u32 s78, s66, 0x8100
	ds_read_b128 v[42:45], v161 offset:16384
	ds_read_b128 v[46:49], v161 offset:17408
	ds_read_b128 v[188:191], v161 offset:18432
	ds_read_b128 v[192:195], v161 offset:19456
	ds_read_b128 v[204:207], v161 offset:20480
	ds_read_b128 v[208:211], v161 offset:21504
	ds_read_b128 v[212:215], v161 offset:22528
	ds_read_b128 v[216:219], v161 offset:23552
	global_load_lds_dwordx4 v[18:19], off
	v_lshl_add_u64 v[18:19], v[152:153], 0, s[24:25]
	s_mov_b32 m0, s76
	s_addc_u32 s79, s67, 0
	s_add_i32 s77, s74, s56
	global_load_lds_dwordx4 v[18:19], off
	v_lshl_add_u64 v[18:19], s[78:79], 0, v[140:141]
	s_mov_b32 m0, s77
	v_lshl_add_u64 v[154:155], s[64:65], 0, v[138:139]
	global_load_lds_dwordx4 v[18:19], off
	v_lshl_add_u64 v[18:19], s[78:79], 0, v[144:145]
	s_add_i32 s78, s77, 0x2000
	s_mov_b32 m0, s78
	v_lshl_add_u64 v[156:157], s[64:65], 0, v[142:143]
	global_load_lds_dwordx4 v[18:19], off
	v_lshl_add_u64 v[18:19], v[154:155], 0, s[24:25]
	s_mov_b32 m0, s51
	s_nop 0
	global_load_lds_dwordx4 v[18:19], off
	v_lshl_add_u64 v[18:19], v[156:157], 0, s[24:25]
	s_mov_b32 m0, s57
	s_nop 0
	global_load_lds_dwordx4 v[18:19], off
	s_waitcnt vmcnt(29)
	s_waitcnt lgkmcnt(0)
	s_barrier
	s_setprio 1
	s_waitcnt lgkmcnt(0)
	v_mfma_f32_16x16x128_f8f6f4 v[86:89], v[10:17], v[42:49], 0
	v_mfma_f32_16x16x128_f8f6f4 v[82:85], v[26:33], v[42:49], 0
	v_mfma_f32_16x16x128_f8f6f4 v[54:57], v[10:17], v[188:195], 0
	v_mfma_f32_16x16x128_f8f6f4 v[50:53], v[26:33], v[188:195], 0
	v_mfma_f32_16x16x128_f8f6f4 v[38:41], v[10:17], v[204:211], 0
	v_mfma_f32_16x16x128_f8f6f4 v[34:37], v[26:33], v[204:211], 0
	v_mfma_f32_16x16x128_f8f6f4 v[22:25], v[10:17], v[212:219], 0
	v_mfma_f32_16x16x128_f8f6f4 v[18:21], v[26:33], v[212:219], 0
	s_setprio 0
	s_setprio 1
	v_mfma_f32_16x16x128_f8f6f4 v[70:73], v[172:179], v[42:49], 0
	v_mfma_f32_16x16x128_f8f6f4 v[66:69], v[180:187], v[42:49], 0
	v_mfma_f32_16x16x128_f8f6f4 v[46:49], v[172:179], v[188:195], 0
	v_mfma_f32_16x16x128_f8f6f4 v[42:45], v[180:187], v[188:195], 0
	v_mfma_f32_16x16x128_f8f6f4 v[30:33], v[172:179], v[204:211], 0
	v_mfma_f32_16x16x128_f8f6f4 v[26:29], v[180:187], v[204:211], 0
	v_mfma_f32_16x16x128_f8f6f4 v[14:17], v[172:179], v[212:219], 0
	v_mfma_f32_16x16x128_f8f6f4 v[10:13], v[180:187], v[212:219], 0
	s_setprio 0
	s_barrier
	s_add_i32 s79, 0, 0x18000
	s_add_i32 s43, 0, 0x1c000
	v_add_u32_e32 v158, s79, v160
	v_add_u32_e32 v159, s43, v160
	ds_read_b128 v[172:175], v158
	ds_read_b128 v[176:179], v158 offset:1024
	ds_read_b128 v[180:183], v158 offset:2048
	ds_read_b128 v[184:187], v158 offset:3072
	ds_read_b128 v[188:191], v159
	ds_read_b128 v[192:195], v159 offset:1024
	ds_read_b128 v[204:207], v159 offset:2048
	ds_read_b128 v[208:211], v159 offset:3072
	s_add_u32 s82, s64, 0x20100
	s_addc_u32 s83, s65, 0
	s_mov_b32 m0, s58
	v_lshl_add_u64 v[196:197], s[82:83], 0, v[138:139]
	ds_read_b128 v[212:215], v161 offset:32768
	ds_read_b128 v[216:219], v161 offset:33792
	ds_read_b128 v[220:223], v161 offset:34816
	ds_read_b128 v[224:227], v161 offset:35840
	ds_read_b128 v[228:231], v161 offset:36864
	ds_read_b128 v[232:235], v161 offset:37888
	ds_read_b128 v[236:239], v161 offset:38912
	ds_read_b128 v[240:243], v161 offset:39936
	global_load_lds_dwordx4 v[196:197], off
	v_lshl_add_u64 v[196:197], s[82:83], 0, v[142:143]
	s_mov_b32 m0, s59
	s_nop 0
	global_load_lds_dwordx4 v[196:197], off
	s_waitcnt vmcnt(29)
	s_waitcnt lgkmcnt(0)
	s_barrier
	s_setprio 1
	s_waitcnt lgkmcnt(0)
	v_mfma_f32_16x16x128_f8f6f4 v[134:137], v[172:179], v[212:219], v[134:137]
	v_mfma_f32_16x16x128_f8f6f4 v[130:133], v[180:187], v[212:219], v[130:133]
	v_mfma_f32_16x16x128_f8f6f4 v[118:121], v[172:179], v[220:227], v[118:121]
	v_mfma_f32_16x16x128_f8f6f4 v[114:117], v[180:187], v[220:227], v[114:117]
	v_mfma_f32_16x16x128_f8f6f4 v[102:105], v[172:179], v[228:235], v[102:105]
	v_mfma_f32_16x16x128_f8f6f4 v[98:101], v[180:187], v[228:235], v[98:101]
	v_mfma_f32_16x16x128_f8f6f4 v[78:81], v[172:179], v[236:243], v[78:81]
	v_mfma_f32_16x16x128_f8f6f4 v[74:77], v[180:187], v[236:243], v[74:77]
	s_setprio 0
	s_setprio 1
	v_mfma_f32_16x16x128_f8f6f4 v[126:129], v[188:195], v[212:219], v[126:129]
	v_mfma_f32_16x16x128_f8f6f4 v[122:125], v[204:211], v[212:219], v[122:125]
	v_mfma_f32_16x16x128_f8f6f4 v[110:113], v[188:195], v[220:227], v[110:113]
	v_mfma_f32_16x16x128_f8f6f4 v[106:109], v[204:211], v[220:227], v[106:109]
	v_mfma_f32_16x16x128_f8f6f4 v[94:97], v[188:195], v[228:235], v[94:97]
	v_mfma_f32_16x16x128_f8f6f4 v[90:93], v[204:211], v[228:235], v[90:93]
	v_mfma_f32_16x16x128_f8f6f4 v[62:65], v[188:195], v[236:243], v[62:65]
	v_mfma_f32_16x16x128_f8f6f4 v[58:61], v[204:211], v[236:243], v[58:61]
	s_setprio 0
	s_barrier
	s_add_i32 s79, s79, s56
	s_add_i32 s41, s79, 0x2000
	v_lshl_add_u64 v[196:197], v[150:151], 0, s[26:27]
	s_mov_b32 m0, s79
	s_add_u32 s82, s66, 0x8180
	ds_read_b128 v[212:215], v161 offset:49152
	ds_read_b128 v[216:219], v161 offset:50176
	ds_read_b128 v[220:223], v161 offset:51200
	ds_read_b128 v[224:227], v161 offset:52224
	ds_read_b128 v[228:231], v161 offset:53248
	ds_read_b128 v[232:235], v161 offset:54272
	ds_read_b128 v[236:239], v161 offset:55296
	ds_read_b128 v[240:243], v161 offset:56320
	global_load_lds_dwordx4 v[196:197], off
	v_lshl_add_u64 v[196:197], v[152:153], 0, s[26:27]
	s_mov_b32 m0, s41
	s_addc_u32 s83, s67, 0
	s_add_i32 s43, s43, s56
	global_load_lds_dwordx4 v[196:197], off
	v_lshl_add_u64 v[196:197], s[82:83], 0, v[140:141]
	s_mov_b32 m0, s43
	s_add_i32 s68, s43, 0x2000
	global_load_lds_dwordx4 v[196:197], off
	v_lshl_add_u64 v[196:197], s[82:83], 0, v[144:145]
	s_mov_b32 m0, s68
	s_nop 0
	global_load_lds_dwordx4 v[196:197], off
	v_lshl_add_u64 v[196:197], v[154:155], 0, s[26:27]
	s_mov_b32 m0, s60
	s_nop 0
	global_load_lds_dwordx4 v[196:197], off
	v_lshl_add_u64 v[196:197], v[156:157], 0, s[26:27]
	s_mov_b32 m0, s61
	s_nop 0
	global_load_lds_dwordx4 v[196:197], off
	s_waitcnt vmcnt(8)
	s_waitcnt lgkmcnt(0)
	s_barrier
	s_setprio 1
	s_waitcnt lgkmcnt(0)
	v_mfma_f32_16x16x128_f8f6f4 v[86:89], v[172:179], v[212:219], v[86:89]
	v_mfma_f32_16x16x128_f8f6f4 v[82:85], v[180:187], v[212:219], v[82:85]
	v_mfma_f32_16x16x128_f8f6f4 v[54:57], v[172:179], v[220:227], v[54:57]
	v_mfma_f32_16x16x128_f8f6f4 v[50:53], v[180:187], v[220:227], v[50:53]
	v_mfma_f32_16x16x128_f8f6f4 v[38:41], v[172:179], v[228:235], v[38:41]
	v_mfma_f32_16x16x128_f8f6f4 v[34:37], v[180:187], v[228:235], v[34:37]
	v_mfma_f32_16x16x128_f8f6f4 v[22:25], v[172:179], v[236:243], v[22:25]
	v_mfma_f32_16x16x128_f8f6f4 v[18:21], v[180:187], v[236:243], v[18:21]
	s_setprio 0
	s_setprio 1
	v_mfma_f32_16x16x128_f8f6f4 v[70:73], v[188:195], v[212:219], v[70:73]
	v_mfma_f32_16x16x128_f8f6f4 v[66:69], v[204:211], v[212:219], v[66:69]
	v_mfma_f32_16x16x128_f8f6f4 v[46:49], v[188:195], v[220:227], v[46:49]
	v_mfma_f32_16x16x128_f8f6f4 v[42:45], v[204:211], v[220:227], v[42:45]
	v_mfma_f32_16x16x128_f8f6f4 v[30:33], v[188:195], v[228:235], v[30:33]
	v_mfma_f32_16x16x128_f8f6f4 v[26:29], v[204:211], v[228:235], v[26:29]
	v_mfma_f32_16x16x128_f8f6f4 v[14:17], v[188:195], v[236:243], v[14:17]
	v_mfma_f32_16x16x128_f8f6f4 v[10:13], v[204:211], v[236:243], v[10:13]
	s_setprio 0
	s_barrier
	ds_read_b128 v[172:175], v162
	ds_read_b128 v[176:179], v162 offset:1024
	ds_read_b128 v[180:183], v162 offset:2048
	ds_read_b128 v[184:187], v162 offset:3072
	ds_read_b128 v[188:191], v163
	ds_read_b128 v[192:195], v163 offset:1024
	ds_read_b128 v[204:207], v163 offset:2048
	ds_read_b128 v[208:211], v163 offset:3072
	s_add_u32 s82, s64, 0x20180
	s_addc_u32 s83, s65, 0
	s_mov_b32 m0, s63
	v_lshl_add_u64 v[196:197], s[82:83], 0, v[138:139]
	ds_read_b128 v[212:215], v161
	ds_read_b128 v[216:219], v161 offset:1024
	ds_read_b128 v[220:223], v161 offset:2048
	ds_read_b128 v[224:227], v161 offset:3072
	ds_read_b128 v[228:231], v161 offset:4096
	ds_read_b128 v[232:235], v161 offset:5120
	ds_read_b128 v[236:239], v161 offset:6144
	ds_read_b128 v[240:243], v161 offset:7168
	global_load_lds_dwordx4 v[196:197], off
	v_lshl_add_u64 v[196:197], s[82:83], 0, v[142:143]
	s_mov_b32 m0, s69
	s_nop 0
	global_load_lds_dwordx4 v[196:197], off
	s_waitcnt vmcnt(8)
	s_waitcnt lgkmcnt(0)
	s_barrier
	s_setprio 1
	s_waitcnt lgkmcnt(0)
	v_mfma_f32_16x16x128_f8f6f4 v[134:137], v[172:179], v[212:219], v[134:137]
	v_mfma_f32_16x16x128_f8f6f4 v[130:133], v[180:187], v[212:219], v[130:133]
	v_mfma_f32_16x16x128_f8f6f4 v[118:121], v[172:179], v[220:227], v[118:121]
	v_mfma_f32_16x16x128_f8f6f4 v[114:117], v[180:187], v[220:227], v[114:117]
	v_mfma_f32_16x16x128_f8f6f4 v[102:105], v[172:179], v[228:235], v[102:105]
	v_mfma_f32_16x16x128_f8f6f4 v[98:101], v[180:187], v[228:235], v[98:101]
	v_mfma_f32_16x16x128_f8f6f4 v[78:81], v[172:179], v[236:243], v[78:81]
	v_mfma_f32_16x16x128_f8f6f4 v[74:77], v[180:187], v[236:243], v[74:77]
	s_setprio 0
	s_setprio 1
	v_mfma_f32_16x16x128_f8f6f4 v[126:129], v[188:195], v[212:219], v[126:129]
	v_mfma_f32_16x16x128_f8f6f4 v[122:125], v[204:211], v[212:219], v[122:125]
	v_mfma_f32_16x16x128_f8f6f4 v[110:113], v[188:195], v[220:227], v[110:113]
	v_mfma_f32_16x16x128_f8f6f4 v[106:109], v[204:211], v[220:227], v[106:109]
	v_mfma_f32_16x16x128_f8f6f4 v[94:97], v[188:195], v[228:235], v[94:97]
	v_mfma_f32_16x16x128_f8f6f4 v[90:93], v[204:211], v[228:235], v[90:93]
	v_mfma_f32_16x16x128_f8f6f4 v[62:65], v[188:195], v[236:243], v[62:65]
	v_mfma_f32_16x16x128_f8f6f4 v[58:61], v[204:211], v[236:243], v[58:61]
	s_setprio 0
	s_barrier
	s_mov_b32 m0, s80
	v_lshl_add_u64 v[196:197], v[150:151], 0, s[28:29]
	s_add_u32 s82, s66, 0x8200
	ds_read_b128 v[212:215], v161 offset:16384
	ds_read_b128 v[216:219], v161 offset:17408
	ds_read_b128 v[220:223], v161 offset:18432
	ds_read_b128 v[224:227], v161 offset:19456
	ds_read_b128 v[228:231], v161 offset:20480
	ds_read_b128 v[232:235], v161 offset:21504
	ds_read_b128 v[236:239], v161 offset:22528
	ds_read_b128 v[240:243], v161 offset:23552
	global_load_lds_dwordx4 v[196:197], off
	v_lshl_add_u64 v[196:197], v[152:153], 0, s[28:29]
	s_mov_b32 m0, s76
	s_addc_u32 s83, s67, 0
	global_load_lds_dwordx4 v[196:197], off
	v_lshl_add_u64 v[196:197], s[82:83], 0, v[140:141]
	s_mov_b32 m0, s77
	s_nop 0
	global_load_lds_dwordx4 v[196:197], off
	v_lshl_add_u64 v[196:197], s[82:83], 0, v[144:145]
	s_mov_b32 m0, s78
	s_nop 0
	global_load_lds_dwordx4 v[196:197], off
	v_lshl_add_u64 v[196:197], v[154:155], 0, s[28:29]
	s_mov_b32 m0, s51
	s_nop 0
	global_load_lds_dwordx4 v[196:197], off
	v_lshl_add_u64 v[196:197], v[156:157], 0, s[28:29]
	s_mov_b32 m0, s57
	s_nop 0
	global_load_lds_dwordx4 v[196:197], off
	s_waitcnt vmcnt(8)
	s_waitcnt lgkmcnt(0)
	s_barrier
	s_setprio 1
	s_waitcnt lgkmcnt(0)
	v_mfma_f32_16x16x128_f8f6f4 v[86:89], v[172:179], v[212:219], v[86:89]
	v_mfma_f32_16x16x128_f8f6f4 v[82:85], v[180:187], v[212:219], v[82:85]
	v_mfma_f32_16x16x128_f8f6f4 v[54:57], v[172:179], v[220:227], v[54:57]
	v_mfma_f32_16x16x128_f8f6f4 v[50:53], v[180:187], v[220:227], v[50:53]
	v_mfma_f32_16x16x128_f8f6f4 v[38:41], v[172:179], v[228:235], v[38:41]
	v_mfma_f32_16x16x128_f8f6f4 v[34:37], v[180:187], v[228:235], v[34:37]
	v_mfma_f32_16x16x128_f8f6f4 v[22:25], v[172:179], v[236:243], v[22:25]
	v_mfma_f32_16x16x128_f8f6f4 v[18:21], v[180:187], v[236:243], v[18:21]
	s_setprio 0
	s_setprio 1
	v_mfma_f32_16x16x128_f8f6f4 v[70:73], v[188:195], v[212:219], v[70:73]
	v_mfma_f32_16x16x128_f8f6f4 v[66:69], v[204:211], v[212:219], v[66:69]
	v_mfma_f32_16x16x128_f8f6f4 v[46:49], v[188:195], v[220:227], v[46:49]
	v_mfma_f32_16x16x128_f8f6f4 v[42:45], v[204:211], v[220:227], v[42:45]
	v_mfma_f32_16x16x128_f8f6f4 v[30:33], v[188:195], v[228:235], v[30:33]
	v_mfma_f32_16x16x128_f8f6f4 v[26:29], v[204:211], v[228:235], v[26:29]
	v_mfma_f32_16x16x128_f8f6f4 v[14:17], v[188:195], v[236:243], v[14:17]
	v_mfma_f32_16x16x128_f8f6f4 v[10:13], v[204:211], v[236:243], v[10:13]
	s_setprio 0
	s_barrier
	ds_read_b128 v[172:175], v158
	ds_read_b128 v[176:179], v158 offset:1024
	ds_read_b128 v[180:183], v158 offset:2048
	ds_read_b128 v[184:187], v158 offset:3072
	ds_read_b128 v[188:191], v159
	ds_read_b128 v[192:195], v159 offset:1024
	ds_read_b128 v[204:207], v159 offset:2048
	ds_read_b128 v[208:211], v159 offset:3072
	s_add_u32 s82, s64, 0x20200
	s_addc_u32 s83, s65, 0
	s_mov_b32 m0, s58
	v_lshl_add_u64 v[196:197], s[82:83], 0, v[138:139]
	ds_read_b128 v[212:215], v161 offset:32768
	ds_read_b128 v[216:219], v161 offset:33792
	ds_read_b128 v[220:223], v161 offset:34816
	ds_read_b128 v[224:227], v161 offset:35840
	ds_read_b128 v[228:231], v161 offset:36864
	ds_read_b128 v[232:235], v161 offset:37888
	ds_read_b128 v[236:239], v161 offset:38912
	ds_read_b128 v[240:243], v161 offset:39936
	global_load_lds_dwordx4 v[196:197], off
	v_lshl_add_u64 v[196:197], s[82:83], 0, v[142:143]
	s_mov_b32 m0, s59
	s_nop 0
	global_load_lds_dwordx4 v[196:197], off
	s_waitcnt vmcnt(8)
	s_waitcnt lgkmcnt(0)
	s_barrier
	s_setprio 1
	s_waitcnt lgkmcnt(0)
	v_mfma_f32_16x16x128_f8f6f4 v[134:137], v[172:179], v[212:219], v[134:137]
	v_mfma_f32_16x16x128_f8f6f4 v[130:133], v[180:187], v[212:219], v[130:133]
	v_mfma_f32_16x16x128_f8f6f4 v[118:121], v[172:179], v[220:227], v[118:121]
	v_mfma_f32_16x16x128_f8f6f4 v[114:117], v[180:187], v[220:227], v[114:117]
	v_mfma_f32_16x16x128_f8f6f4 v[102:105], v[172:179], v[228:235], v[102:105]
	v_mfma_f32_16x16x128_f8f6f4 v[98:101], v[180:187], v[228:235], v[98:101]
	v_mfma_f32_16x16x128_f8f6f4 v[78:81], v[172:179], v[236:243], v[78:81]
	v_mfma_f32_16x16x128_f8f6f4 v[74:77], v[180:187], v[236:243], v[74:77]
	s_setprio 0
	s_setprio 1
	v_mfma_f32_16x16x128_f8f6f4 v[126:129], v[188:195], v[212:219], v[126:129]
	v_mfma_f32_16x16x128_f8f6f4 v[122:125], v[204:211], v[212:219], v[122:125]
	v_mfma_f32_16x16x128_f8f6f4 v[110:113], v[188:195], v[220:227], v[110:113]
	v_mfma_f32_16x16x128_f8f6f4 v[106:109], v[204:211], v[220:227], v[106:109]
	v_mfma_f32_16x16x128_f8f6f4 v[94:97], v[188:195], v[228:235], v[94:97]
	v_mfma_f32_16x16x128_f8f6f4 v[90:93], v[204:211], v[228:235], v[90:93]
	v_mfma_f32_16x16x128_f8f6f4 v[62:65], v[188:195], v[236:243], v[62:65]
	v_mfma_f32_16x16x128_f8f6f4 v[58:61], v[204:211], v[236:243], v[58:61]
	s_setprio 0
	s_barrier
	s_mov_b32 m0, s79
	v_lshl_add_u64 v[196:197], v[150:151], 0, s[30:31]
	s_add_u32 s82, s66, 0x8280
	ds_read_b128 v[212:215], v161 offset:49152
	ds_read_b128 v[216:219], v161 offset:50176
	ds_read_b128 v[220:223], v161 offset:51200
	ds_read_b128 v[224:227], v161 offset:52224
	ds_read_b128 v[228:231], v161 offset:53248
	ds_read_b128 v[232:235], v161 offset:54272
	ds_read_b128 v[236:239], v161 offset:55296
	ds_read_b128 v[240:243], v161 offset:56320
	global_load_lds_dwordx4 v[196:197], off
	v_lshl_add_u64 v[196:197], v[152:153], 0, s[30:31]
	s_mov_b32 m0, s41
	s_addc_u32 s83, s67, 0
	global_load_lds_dwordx4 v[196:197], off
	v_lshl_add_u64 v[196:197], s[82:83], 0, v[140:141]
	s_mov_b32 m0, s43
	s_nop 0
	global_load_lds_dwordx4 v[196:197], off
	v_lshl_add_u64 v[196:197], s[82:83], 0, v[144:145]
	s_mov_b32 m0, s68
	s_nop 0
	global_load_lds_dwordx4 v[196:197], off
	v_lshl_add_u64 v[196:197], v[154:155], 0, s[30:31]
	s_mov_b32 m0, s60
	s_nop 0
	global_load_lds_dwordx4 v[196:197], off
	v_lshl_add_u64 v[196:197], v[156:157], 0, s[30:31]
	s_mov_b32 m0, s61
	s_nop 0
	global_load_lds_dwordx4 v[196:197], off
	s_waitcnt vmcnt(8)
	s_waitcnt lgkmcnt(0)
	s_barrier
	s_setprio 1
	s_waitcnt lgkmcnt(0)
	v_mfma_f32_16x16x128_f8f6f4 v[86:89], v[172:179], v[212:219], v[86:89]
	v_mfma_f32_16x16x128_f8f6f4 v[82:85], v[180:187], v[212:219], v[82:85]
	v_mfma_f32_16x16x128_f8f6f4 v[54:57], v[172:179], v[220:227], v[54:57]
	v_mfma_f32_16x16x128_f8f6f4 v[50:53], v[180:187], v[220:227], v[50:53]
	v_mfma_f32_16x16x128_f8f6f4 v[38:41], v[172:179], v[228:235], v[38:41]
	v_mfma_f32_16x16x128_f8f6f4 v[34:37], v[180:187], v[228:235], v[34:37]
	v_mfma_f32_16x16x128_f8f6f4 v[22:25], v[172:179], v[236:243], v[22:25]
	v_mfma_f32_16x16x128_f8f6f4 v[18:21], v[180:187], v[236:243], v[18:21]
	s_setprio 0
	s_setprio 1
	v_mfma_f32_16x16x128_f8f6f4 v[70:73], v[188:195], v[212:219], v[70:73]
	v_mfma_f32_16x16x128_f8f6f4 v[66:69], v[204:211], v[212:219], v[66:69]
	v_mfma_f32_16x16x128_f8f6f4 v[46:49], v[188:195], v[220:227], v[46:49]
	v_mfma_f32_16x16x128_f8f6f4 v[42:45], v[204:211], v[220:227], v[42:45]
	v_mfma_f32_16x16x128_f8f6f4 v[30:33], v[188:195], v[228:235], v[30:33]
	v_mfma_f32_16x16x128_f8f6f4 v[26:29], v[204:211], v[228:235], v[26:29]
	v_mfma_f32_16x16x128_f8f6f4 v[14:17], v[188:195], v[236:243], v[14:17]
	v_mfma_f32_16x16x128_f8f6f4 v[10:13], v[204:211], v[236:243], v[10:13]
	s_setprio 0
	s_barrier
	ds_read_b128 v[172:175], v162
	ds_read_b128 v[176:179], v162 offset:1024
	ds_read_b128 v[180:183], v162 offset:2048
	ds_read_b128 v[184:187], v162 offset:3072
	ds_read_b128 v[188:191], v163
	ds_read_b128 v[192:195], v163 offset:1024
	ds_read_b128 v[204:207], v163 offset:2048
	ds_read_b128 v[208:211], v163 offset:3072
	s_add_u32 s82, s64, 0x20280
	s_addc_u32 s83, s65, 0
	s_mov_b32 m0, s63
	v_lshl_add_u64 v[196:197], s[82:83], 0, v[138:139]
	ds_read_b128 v[212:215], v161
	ds_read_b128 v[216:219], v161 offset:1024
	ds_read_b128 v[220:223], v161 offset:2048
	ds_read_b128 v[224:227], v161 offset:3072
	ds_read_b128 v[228:231], v161 offset:4096
	ds_read_b128 v[232:235], v161 offset:5120
	ds_read_b128 v[236:239], v161 offset:6144
	ds_read_b128 v[240:243], v161 offset:7168
	global_load_lds_dwordx4 v[196:197], off
	v_lshl_add_u64 v[196:197], s[82:83], 0, v[142:143]
	s_mov_b32 m0, s69
	s_nop 0
	global_load_lds_dwordx4 v[196:197], off
	s_waitcnt vmcnt(8)
	s_waitcnt lgkmcnt(0)
	s_barrier
	s_setprio 1
	s_waitcnt lgkmcnt(0)
	v_mfma_f32_16x16x128_f8f6f4 v[134:137], v[172:179], v[212:219], v[134:137]
	v_mfma_f32_16x16x128_f8f6f4 v[130:133], v[180:187], v[212:219], v[130:133]
	v_mfma_f32_16x16x128_f8f6f4 v[118:121], v[172:179], v[220:227], v[118:121]
	v_mfma_f32_16x16x128_f8f6f4 v[114:117], v[180:187], v[220:227], v[114:117]
	v_mfma_f32_16x16x128_f8f6f4 v[102:105], v[172:179], v[228:235], v[102:105]
	v_mfma_f32_16x16x128_f8f6f4 v[98:101], v[180:187], v[228:235], v[98:101]
	v_mfma_f32_16x16x128_f8f6f4 v[78:81], v[172:179], v[236:243], v[78:81]
	v_mfma_f32_16x16x128_f8f6f4 v[74:77], v[180:187], v[236:243], v[74:77]
	s_setprio 0
	s_setprio 1
	v_mfma_f32_16x16x128_f8f6f4 v[126:129], v[188:195], v[212:219], v[126:129]
	v_mfma_f32_16x16x128_f8f6f4 v[122:125], v[204:211], v[212:219], v[122:125]
	v_mfma_f32_16x16x128_f8f6f4 v[110:113], v[188:195], v[220:227], v[110:113]
	v_mfma_f32_16x16x128_f8f6f4 v[106:109], v[204:211], v[220:227], v[106:109]
	v_mfma_f32_16x16x128_f8f6f4 v[94:97], v[188:195], v[228:235], v[94:97]
	v_mfma_f32_16x16x128_f8f6f4 v[90:93], v[204:211], v[228:235], v[90:93]
	v_mfma_f32_16x16x128_f8f6f4 v[62:65], v[188:195], v[236:243], v[62:65]
	v_mfma_f32_16x16x128_f8f6f4 v[58:61], v[204:211], v[236:243], v[58:61]
	s_setprio 0
	s_barrier
	s_mov_b32 m0, s80
	v_lshl_add_u64 v[196:197], v[150:151], 0, s[34:35]
	s_add_u32 s82, s66, 0x8300
	ds_read_b128 v[212:215], v161 offset:16384
	ds_read_b128 v[216:219], v161 offset:17408
	ds_read_b128 v[220:223], v161 offset:18432
	ds_read_b128 v[224:227], v161 offset:19456
	ds_read_b128 v[228:231], v161 offset:20480
	ds_read_b128 v[232:235], v161 offset:21504
	ds_read_b128 v[236:239], v161 offset:22528
	ds_read_b128 v[240:243], v161 offset:23552
	global_load_lds_dwordx4 v[196:197], off
	v_lshl_add_u64 v[196:197], v[152:153], 0, s[34:35]
	s_mov_b32 m0, s76
	s_addc_u32 s83, s67, 0
	global_load_lds_dwordx4 v[196:197], off
	v_lshl_add_u64 v[196:197], s[82:83], 0, v[140:141]
	s_mov_b32 m0, s77
	s_nop 0
	global_load_lds_dwordx4 v[196:197], off
	v_lshl_add_u64 v[196:197], s[82:83], 0, v[144:145]
	s_mov_b32 m0, s78
	s_nop 0
	global_load_lds_dwordx4 v[196:197], off
	v_lshl_add_u64 v[196:197], v[154:155], 0, s[34:35]
	s_mov_b32 m0, s51
	s_nop 0
	global_load_lds_dwordx4 v[196:197], off
	v_lshl_add_u64 v[196:197], v[156:157], 0, s[34:35]
	s_mov_b32 m0, s57
	s_nop 0
	global_load_lds_dwordx4 v[196:197], off
	s_waitcnt vmcnt(8)
	s_waitcnt lgkmcnt(0)
	s_barrier
	s_setprio 1
	s_waitcnt lgkmcnt(0)
	v_mfma_f32_16x16x128_f8f6f4 v[86:89], v[172:179], v[212:219], v[86:89]
	v_mfma_f32_16x16x128_f8f6f4 v[82:85], v[180:187], v[212:219], v[82:85]
	v_mfma_f32_16x16x128_f8f6f4 v[54:57], v[172:179], v[220:227], v[54:57]
	v_mfma_f32_16x16x128_f8f6f4 v[50:53], v[180:187], v[220:227], v[50:53]
	v_mfma_f32_16x16x128_f8f6f4 v[38:41], v[172:179], v[228:235], v[38:41]
	v_mfma_f32_16x16x128_f8f6f4 v[34:37], v[180:187], v[228:235], v[34:37]
	v_mfma_f32_16x16x128_f8f6f4 v[22:25], v[172:179], v[236:243], v[22:25]
	v_mfma_f32_16x16x128_f8f6f4 v[18:21], v[180:187], v[236:243], v[18:21]
	s_setprio 0
	s_setprio 1
	v_mfma_f32_16x16x128_f8f6f4 v[70:73], v[188:195], v[212:219], v[70:73]
	v_mfma_f32_16x16x128_f8f6f4 v[66:69], v[204:211], v[212:219], v[66:69]
	v_mfma_f32_16x16x128_f8f6f4 v[46:49], v[188:195], v[220:227], v[46:49]
	v_mfma_f32_16x16x128_f8f6f4 v[42:45], v[204:211], v[220:227], v[42:45]
	v_mfma_f32_16x16x128_f8f6f4 v[30:33], v[188:195], v[228:235], v[30:33]
	v_mfma_f32_16x16x128_f8f6f4 v[26:29], v[204:211], v[228:235], v[26:29]
	v_mfma_f32_16x16x128_f8f6f4 v[14:17], v[188:195], v[236:243], v[14:17]
	v_mfma_f32_16x16x128_f8f6f4 v[10:13], v[204:211], v[236:243], v[10:13]
	s_setprio 0
	s_barrier
	ds_read_b128 v[172:175], v158
	ds_read_b128 v[176:179], v158 offset:1024
	ds_read_b128 v[180:183], v158 offset:2048
	ds_read_b128 v[184:187], v158 offset:3072
	ds_read_b128 v[188:191], v159
	ds_read_b128 v[192:195], v159 offset:1024
	ds_read_b128 v[204:207], v159 offset:2048
	ds_read_b128 v[208:211], v159 offset:3072
	s_add_u32 s82, s64, 0x20300
	s_addc_u32 s83, s65, 0
	s_mov_b32 m0, s58
	v_lshl_add_u64 v[196:197], s[82:83], 0, v[138:139]
	ds_read_b128 v[212:215], v161 offset:32768
	ds_read_b128 v[216:219], v161 offset:33792
	ds_read_b128 v[220:223], v161 offset:34816
	ds_read_b128 v[224:227], v161 offset:35840
	ds_read_b128 v[228:231], v161 offset:36864
	ds_read_b128 v[232:235], v161 offset:37888
	ds_read_b128 v[236:239], v161 offset:38912
	ds_read_b128 v[240:243], v161 offset:39936
	global_load_lds_dwordx4 v[196:197], off
	v_lshl_add_u64 v[196:197], s[82:83], 0, v[142:143]
	s_mov_b32 m0, s59
	s_nop 0
	global_load_lds_dwordx4 v[196:197], off
	s_waitcnt vmcnt(8)
	s_waitcnt lgkmcnt(0)
	s_barrier
	s_setprio 1
	s_waitcnt lgkmcnt(0)
	v_mfma_f32_16x16x128_f8f6f4 v[134:137], v[172:179], v[212:219], v[134:137]
	v_mfma_f32_16x16x128_f8f6f4 v[130:133], v[180:187], v[212:219], v[130:133]
	v_mfma_f32_16x16x128_f8f6f4 v[118:121], v[172:179], v[220:227], v[118:121]
	v_mfma_f32_16x16x128_f8f6f4 v[114:117], v[180:187], v[220:227], v[114:117]
	v_mfma_f32_16x16x128_f8f6f4 v[102:105], v[172:179], v[228:235], v[102:105]
	v_mfma_f32_16x16x128_f8f6f4 v[98:101], v[180:187], v[228:235], v[98:101]
	v_mfma_f32_16x16x128_f8f6f4 v[78:81], v[172:179], v[236:243], v[78:81]
	v_mfma_f32_16x16x128_f8f6f4 v[74:77], v[180:187], v[236:243], v[74:77]
	s_setprio 0
	s_setprio 1
	v_mfma_f32_16x16x128_f8f6f4 v[126:129], v[188:195], v[212:219], v[126:129]
	v_mfma_f32_16x16x128_f8f6f4 v[122:125], v[204:211], v[212:219], v[122:125]
	v_mfma_f32_16x16x128_f8f6f4 v[110:113], v[188:195], v[220:227], v[110:113]
	v_mfma_f32_16x16x128_f8f6f4 v[106:109], v[204:211], v[220:227], v[106:109]
	v_mfma_f32_16x16x128_f8f6f4 v[94:97], v[188:195], v[228:235], v[94:97]
	v_mfma_f32_16x16x128_f8f6f4 v[90:93], v[204:211], v[228:235], v[90:93]
	v_mfma_f32_16x16x128_f8f6f4 v[62:65], v[188:195], v[236:243], v[62:65]
	v_mfma_f32_16x16x128_f8f6f4 v[58:61], v[204:211], v[236:243], v[58:61]
	s_setprio 0
	s_barrier
	s_mov_b32 m0, s79
	v_lshl_add_u64 v[150:151], v[150:151], 0, s[36:37]
	s_add_u32 s66, s66, 0x8380
	ds_read_b128 v[212:215], v161 offset:49152
	ds_read_b128 v[216:219], v161 offset:50176
	ds_read_b128 v[220:223], v161 offset:51200
	ds_read_b128 v[224:227], v161 offset:52224
	ds_read_b128 v[228:231], v161 offset:53248
	ds_read_b128 v[232:235], v161 offset:54272
	ds_read_b128 v[236:239], v161 offset:55296
	ds_read_b128 v[240:243], v161 offset:56320
	global_load_lds_dwordx4 v[150:151], off
	v_lshl_add_u64 v[150:151], v[152:153], 0, s[36:37]
	s_mov_b32 m0, s41
	s_addc_u32 s67, s67, 0
	global_load_lds_dwordx4 v[150:151], off
	v_lshl_add_u64 v[150:151], s[66:67], 0, v[140:141]
	s_mov_b32 m0, s43
	s_nop 0
	global_load_lds_dwordx4 v[150:151], off
	v_lshl_add_u64 v[150:151], s[66:67], 0, v[144:145]
	s_mov_b32 m0, s68
	s_nop 0
	global_load_lds_dwordx4 v[150:151], off
	v_lshl_add_u64 v[150:151], v[154:155], 0, s[36:37]
	s_mov_b32 m0, s60
	s_nop 0
	global_load_lds_dwordx4 v[150:151], off
	v_lshl_add_u64 v[150:151], v[156:157], 0, s[36:37]
	s_mov_b32 m0, s61
	s_nop 0
	global_load_lds_dwordx4 v[150:151], off
	s_waitcnt vmcnt(8)
	s_waitcnt lgkmcnt(0)
	s_barrier
	s_setprio 1
	s_waitcnt lgkmcnt(0)
	v_mfma_f32_16x16x128_f8f6f4 v[86:89], v[172:179], v[212:219], v[86:89]
	v_mfma_f32_16x16x128_f8f6f4 v[82:85], v[180:187], v[212:219], v[82:85]
	v_mfma_f32_16x16x128_f8f6f4 v[54:57], v[172:179], v[220:227], v[54:57]
	v_mfma_f32_16x16x128_f8f6f4 v[50:53], v[180:187], v[220:227], v[50:53]
	v_mfma_f32_16x16x128_f8f6f4 v[38:41], v[172:179], v[228:235], v[38:41]
	v_mfma_f32_16x16x128_f8f6f4 v[34:37], v[180:187], v[228:235], v[34:37]
	v_mfma_f32_16x16x128_f8f6f4 v[22:25], v[172:179], v[236:243], v[22:25]
	v_mfma_f32_16x16x128_f8f6f4 v[18:21], v[180:187], v[236:243], v[18:21]
	s_setprio 0
	s_setprio 1
	v_mfma_f32_16x16x128_f8f6f4 v[70:73], v[188:195], v[212:219], v[70:73]
	v_mfma_f32_16x16x128_f8f6f4 v[66:69], v[204:211], v[212:219], v[66:69]
	v_mfma_f32_16x16x128_f8f6f4 v[46:49], v[188:195], v[220:227], v[46:49]
	v_mfma_f32_16x16x128_f8f6f4 v[42:45], v[204:211], v[220:227], v[42:45]
	v_mfma_f32_16x16x128_f8f6f4 v[30:33], v[188:195], v[228:235], v[30:33]
	v_mfma_f32_16x16x128_f8f6f4 v[26:29], v[204:211], v[228:235], v[26:29]
	v_mfma_f32_16x16x128_f8f6f4 v[14:17], v[188:195], v[236:243], v[14:17]
	v_mfma_f32_16x16x128_f8f6f4 v[10:13], v[204:211], v[236:243], v[10:13]
	s_setprio 0
	s_barrier
	ds_read_b128 v[150:153], v162
	ds_read_b128 v[154:157], v162 offset:1024
	ds_read_b128 v[172:175], v162 offset:2048
	ds_read_b128 v[176:179], v162 offset:3072
	ds_read_b128 v[180:183], v163
	ds_read_b128 v[184:187], v163 offset:1024
	ds_read_b128 v[188:191], v163 offset:2048
	ds_read_b128 v[192:195], v163 offset:3072
	s_add_u32 s64, s64, 0x20380
	s_addc_u32 s65, s65, 0
	s_mov_b32 m0, s63
	v_lshl_add_u64 v[196:197], s[64:65], 0, v[138:139]
	ds_read_b128 v[204:207], v161
	ds_read_b128 v[208:211], v161 offset:1024
	ds_read_b128 v[212:215], v161 offset:2048
	ds_read_b128 v[216:219], v161 offset:3072
	ds_read_b128 v[220:223], v161 offset:4096
	ds_read_b128 v[224:227], v161 offset:5120
	ds_read_b128 v[228:231], v161 offset:6144
	ds_read_b128 v[232:235], v161 offset:7168
	global_load_lds_dwordx4 v[196:197], off
	v_lshl_add_u64 v[196:197], s[64:65], 0, v[142:143]
	s_mov_b32 m0, s69
	s_nop 0
	global_load_lds_dwordx4 v[196:197], off
	s_waitcnt vmcnt(8)
	s_waitcnt lgkmcnt(0)
	s_barrier
	s_setprio 1
	s_waitcnt lgkmcnt(0)
	v_mfma_f32_16x16x128_f8f6f4 v[134:137], v[150:157], v[204:211], v[134:137]
	v_mfma_f32_16x16x128_f8f6f4 v[130:133], v[172:179], v[204:211], v[130:133]
	v_mfma_f32_16x16x128_f8f6f4 v[118:121], v[150:157], v[212:219], v[118:121]
	v_mfma_f32_16x16x128_f8f6f4 v[114:117], v[172:179], v[212:219], v[114:117]
	v_mfma_f32_16x16x128_f8f6f4 v[102:105], v[150:157], v[220:227], v[102:105]
	v_mfma_f32_16x16x128_f8f6f4 v[98:101], v[172:179], v[220:227], v[98:101]
	v_mfma_f32_16x16x128_f8f6f4 v[78:81], v[150:157], v[228:235], v[78:81]
	v_mfma_f32_16x16x128_f8f6f4 v[74:77], v[172:179], v[228:235], v[74:77]
	s_setprio 0
	s_setprio 1
	v_mfma_f32_16x16x128_f8f6f4 v[126:129], v[180:187], v[204:211], v[126:129]
	v_mfma_f32_16x16x128_f8f6f4 v[122:125], v[188:195], v[204:211], v[122:125]
	v_mfma_f32_16x16x128_f8f6f4 v[110:113], v[180:187], v[212:219], v[110:113]
	v_mfma_f32_16x16x128_f8f6f4 v[106:109], v[188:195], v[212:219], v[106:109]
	v_mfma_f32_16x16x128_f8f6f4 v[94:97], v[180:187], v[220:227], v[94:97]
	v_mfma_f32_16x16x128_f8f6f4 v[90:93], v[188:195], v[220:227], v[90:93]
	v_mfma_f32_16x16x128_f8f6f4 v[62:65], v[180:187], v[228:235], v[62:65]
	v_mfma_f32_16x16x128_f8f6f4 v[58:61], v[188:195], v[228:235], v[58:61]
	s_setprio 0
	s_barrier
	s_mov_b32 m0, s80
	v_lshl_add_u64 v[196:197], s[10:11], 0, v[140:141]
	s_add_u32 s64, s10, 0x8000
	ds_read_b128 v[204:207], v161 offset:16384
	ds_read_b128 v[208:211], v161 offset:17408
	ds_read_b128 v[212:215], v161 offset:18432
	ds_read_b128 v[216:219], v161 offset:19456
	ds_read_b128 v[220:223], v161 offset:20480
	ds_read_b128 v[224:227], v161 offset:21504
	ds_read_b128 v[228:231], v161 offset:22528
	ds_read_b128 v[232:235], v161 offset:23552
	global_load_lds_dwordx4 v[196:197], off
	v_lshl_add_u64 v[198:199], s[10:11], 0, v[144:145]
	s_mov_b32 m0, s76
	s_addc_u32 s65, s11, 0
	global_load_lds_dwordx4 v[198:199], off
	v_lshl_add_u64 v[200:201], s[64:65], 0, v[140:141]
	s_mov_b32 m0, s77
	v_lshl_add_u64 v[236:237], s[70:71], 0, v[142:143]
	global_load_lds_dwordx4 v[200:201], off
	v_lshl_add_u64 v[200:201], s[64:65], 0, v[144:145]
	s_mov_b32 m0, s78
	s_nop 0
	global_load_lds_dwordx4 v[200:201], off
	v_lshl_add_u64 v[200:201], s[70:71], 0, v[138:139]
	s_mov_b32 m0, s51
	s_nop 0
	global_load_lds_dwordx4 v[200:201], off
	s_mov_b32 m0, s57
	s_nop 0
	global_load_lds_dwordx4 v[236:237], off
	s_waitcnt vmcnt(8)
	s_waitcnt lgkmcnt(0)
	s_barrier
	s_setprio 1
	s_waitcnt lgkmcnt(0)
	v_mfma_f32_16x16x128_f8f6f4 v[86:89], v[150:157], v[204:211], v[86:89]
	v_mfma_f32_16x16x128_f8f6f4 v[82:85], v[172:179], v[204:211], v[82:85]
	v_mfma_f32_16x16x128_f8f6f4 v[54:57], v[150:157], v[212:219], v[54:57]
	v_mfma_f32_16x16x128_f8f6f4 v[50:53], v[172:179], v[212:219], v[50:53]
	v_mfma_f32_16x16x128_f8f6f4 v[38:41], v[150:157], v[220:227], v[38:41]
	v_mfma_f32_16x16x128_f8f6f4 v[34:37], v[172:179], v[220:227], v[34:37]
	v_mfma_f32_16x16x128_f8f6f4 v[22:25], v[150:157], v[228:235], v[22:25]
	v_mfma_f32_16x16x128_f8f6f4 v[18:21], v[172:179], v[228:235], v[18:21]
	s_setprio 0
	s_setprio 1
	v_mfma_f32_16x16x128_f8f6f4 v[70:73], v[180:187], v[204:211], v[70:73]
	v_mfma_f32_16x16x128_f8f6f4 v[66:69], v[188:195], v[204:211], v[66:69]
	v_mfma_f32_16x16x128_f8f6f4 v[46:49], v[180:187], v[212:219], v[46:49]
	v_mfma_f32_16x16x128_f8f6f4 v[42:45], v[188:195], v[212:219], v[42:45]
	v_mfma_f32_16x16x128_f8f6f4 v[30:33], v[180:187], v[220:227], v[30:33]
	v_mfma_f32_16x16x128_f8f6f4 v[26:29], v[188:195], v[220:227], v[26:29]
	v_mfma_f32_16x16x128_f8f6f4 v[14:17], v[180:187], v[228:235], v[14:17]
	v_mfma_f32_16x16x128_f8f6f4 v[10:13], v[188:195], v[228:235], v[10:13]
	s_setprio 0
	s_barrier
	ds_read_b128 v[150:153], v158
	ds_read_b128 v[154:157], v158 offset:1024
	ds_read_b128 v[172:175], v158 offset:2048
	ds_read_b128 v[176:179], v158 offset:3072
	ds_read_b128 v[180:183], v159
	ds_read_b128 v[184:187], v159 offset:1024
	ds_read_b128 v[188:191], v159 offset:2048
	ds_read_b128 v[192:195], v159 offset:3072
	s_add_u32 s64, s70, 0x20000
	s_addc_u32 s65, s71, 0
	s_mov_b32 m0, s58
	v_lshl_add_u64 v[158:159], s[64:65], 0, v[138:139]
	ds_read_b128 v[204:207], v161 offset:32768
	ds_read_b128 v[208:211], v161 offset:33792
	ds_read_b128 v[212:215], v161 offset:34816
	ds_read_b128 v[216:219], v161 offset:35840
	ds_read_b128 v[220:223], v161 offset:36864
	ds_read_b128 v[224:227], v161 offset:37888
	ds_read_b128 v[228:231], v161 offset:38912
	ds_read_b128 v[232:235], v161 offset:39936
	global_load_lds_dwordx4 v[158:159], off
	v_lshl_add_u64 v[158:159], s[64:65], 0, v[142:143]
	s_mov_b32 m0, s59
	s_nop 0
	global_load_lds_dwordx4 v[158:159], off
	s_waitcnt vmcnt(8)
	s_waitcnt lgkmcnt(0)
	s_barrier
	s_setprio 1
	s_waitcnt lgkmcnt(0)
	v_mfma_f32_16x16x128_f8f6f4 v[134:137], v[150:157], v[204:211], v[134:137]
	v_mfma_f32_16x16x128_f8f6f4 v[130:133], v[172:179], v[204:211], v[130:133]
	v_mfma_f32_16x16x128_f8f6f4 v[118:121], v[150:157], v[212:219], v[118:121]
	v_mfma_f32_16x16x128_f8f6f4 v[114:117], v[172:179], v[212:219], v[114:117]
	v_mfma_f32_16x16x128_f8f6f4 v[102:105], v[150:157], v[220:227], v[102:105]
	v_mfma_f32_16x16x128_f8f6f4 v[98:101], v[172:179], v[220:227], v[98:101]
	v_mfma_f32_16x16x128_f8f6f4 v[78:81], v[150:157], v[228:235], v[78:81]
	v_mfma_f32_16x16x128_f8f6f4 v[74:77], v[172:179], v[228:235], v[74:77]
	s_setprio 0
	s_setprio 1
	v_mfma_f32_16x16x128_f8f6f4 v[126:129], v[180:187], v[204:211], v[126:129]
	v_mfma_f32_16x16x128_f8f6f4 v[122:125], v[188:195], v[204:211], v[122:125]
	v_mfma_f32_16x16x128_f8f6f4 v[110:113], v[180:187], v[212:219], v[110:113]
	v_mfma_f32_16x16x128_f8f6f4 v[106:109], v[188:195], v[212:219], v[106:109]
	v_mfma_f32_16x16x128_f8f6f4 v[94:97], v[180:187], v[220:227], v[94:97]
	v_mfma_f32_16x16x128_f8f6f4 v[90:93], v[188:195], v[220:227], v[90:93]
	v_mfma_f32_16x16x128_f8f6f4 v[62:65], v[180:187], v[228:235], v[62:65]
	v_mfma_f32_16x16x128_f8f6f4 v[58:61], v[188:195], v[228:235], v[58:61]
	s_setprio 0
	s_barrier
	s_mov_b32 m0, s79
	v_lshl_add_u64 v[158:159], v[196:197], 0, s[18:19]
	s_add_u32 s10, s10, 0x8080
	ds_read_b128 v[204:207], v161 offset:49152
	ds_read_b128 v[208:211], v161 offset:50176
	ds_read_b128 v[212:215], v161 offset:51200
	ds_read_b128 v[216:219], v161 offset:52224
	ds_read_b128 v[220:223], v161 offset:53248
	ds_read_b128 v[224:227], v161 offset:54272
	ds_read_b128 v[228:231], v161 offset:55296
	ds_read_b128 v[232:235], v161 offset:56320
	global_load_lds_dwordx4 v[158:159], off
	v_lshl_add_u64 v[158:159], v[198:199], 0, s[18:19]
	s_mov_b32 m0, s41
	s_addc_u32 s11, s11, 0
	global_load_lds_dwordx4 v[158:159], off
	v_lshl_add_u64 v[158:159], s[10:11], 0, v[140:141]
	s_mov_b32 m0, s43
	s_nop 0
	global_load_lds_dwordx4 v[158:159], off
	v_lshl_add_u64 v[158:159], s[10:11], 0, v[144:145]
	s_mov_b32 m0, s68
	s_nop 0
	global_load_lds_dwordx4 v[158:159], off
	v_lshl_add_u64 v[158:159], v[200:201], 0, s[18:19]
	s_mov_b32 m0, s60
	s_nop 0
	global_load_lds_dwordx4 v[158:159], off
	v_lshl_add_u64 v[158:159], v[236:237], 0, s[18:19]
	s_mov_b32 m0, s61
	s_nop 0
	global_load_lds_dwordx4 v[158:159], off
	s_waitcnt vmcnt(8)
	s_waitcnt lgkmcnt(0)
	s_barrier
	s_setprio 1
	s_waitcnt lgkmcnt(0)
	v_mfma_f32_16x16x128_f8f6f4 v[86:89], v[150:157], v[204:211], v[86:89]
	v_mfma_f32_16x16x128_f8f6f4 v[82:85], v[172:179], v[204:211], v[82:85]
	v_mfma_f32_16x16x128_f8f6f4 v[54:57], v[150:157], v[212:219], v[54:57]
	v_mfma_f32_16x16x128_f8f6f4 v[50:53], v[172:179], v[212:219], v[50:53]
	v_mfma_f32_16x16x128_f8f6f4 v[38:41], v[150:157], v[220:227], v[38:41]
	v_mfma_f32_16x16x128_f8f6f4 v[34:37], v[172:179], v[220:227], v[34:37]
	v_mfma_f32_16x16x128_f8f6f4 v[22:25], v[150:157], v[228:235], v[22:25]
	v_mfma_f32_16x16x128_f8f6f4 v[18:21], v[172:179], v[228:235], v[18:21]
	s_setprio 0
	s_setprio 1
	v_mfma_f32_16x16x128_f8f6f4 v[70:73], v[180:187], v[204:211], v[70:73]
	v_mfma_f32_16x16x128_f8f6f4 v[66:69], v[188:195], v[204:211], v[66:69]
	v_mfma_f32_16x16x128_f8f6f4 v[46:49], v[180:187], v[212:219], v[46:49]
	v_mfma_f32_16x16x128_f8f6f4 v[42:45], v[188:195], v[212:219], v[42:45]
	v_mfma_f32_16x16x128_f8f6f4 v[30:33], v[180:187], v[220:227], v[30:33]
	v_mfma_f32_16x16x128_f8f6f4 v[26:29], v[188:195], v[220:227], v[26:29]
	v_mfma_f32_16x16x128_f8f6f4 v[14:17], v[180:187], v[228:235], v[14:17]
	v_mfma_f32_16x16x128_f8f6f4 v[10:13], v[188:195], v[228:235], v[10:13]
	s_setprio 0
	s_barrier
	v_cndmask_b32_e64 v150, 0, 1, s[8:9]
	v_cmp_ne_u32_e64 s[10:11], 1, v150
	s_andn2_b64 vcc, exec, s[8:9]
	s_cbranch_vccnz .LBB0_3427
	s_add_u32 s8, s46, 0x20080
	s_addc_u32 s9, s47, 0
	s_mov_b32 m0, s63
	v_lshl_add_u64 v[150:151], s[8:9], 0, v[138:139]
	v_lshl_add_u64 v[152:153], s[8:9], 0, v[142:143]
	global_load_lds_dwordx4 v[150:151], off
	s_mov_b32 m0, s69
	s_nop 0
	global_load_lds_dwordx4 v[152:153], off

.LBB0_3429:
	s_cmp_lg_u64 s[10:11], 0
	s_cbranch_scc1 .Ldpf_skip_1
	v_lshrrev_b32_e32 v244, 1, v0
	v_and_b32_e32 v245, 1, v0
	v_lshlrev_b32_e32 v244, 10, v244
	v_lshl_add_u32 v244, v245, 7, v244
	s_add_u32 s92, s46, 0x100
	s_addc_u32 s93, s47, 0
	global_load_dword v246, v244, s[92:93]
	global_load_dword v247, v244, s[92:93] offset:256
	global_load_dword v248, v244, s[92:93] offset:512
.Ldpf_skip_1:
	v_lshlrev_b32_e32 v158, 16, v6
	v_and_b32_e32 v159, 0xffff0000, v6
	v_lshlrev_b32_e32 v154, 16, v8
	v_and_b32_e32 v155, 0xffff0000, v8
	v_lshlrev_b32_e32 v156, 16, v7
	v_and_b32_e32 v157, 0xffff0000, v7
	v_lshlrev_b32_e32 v152, 16, v9
	v_and_b32_e32 v153, 0xffff0000, v9
	s_waitcnt vmcnt(13)
	v_lshlrev_b32_e32 v6, 16, v4
	v_and_b32_e32 v7, 0xffff0000, v4
	v_mul_f32_e32 v4, 0x41000000, v146
	v_pk_fma_f32 v[134:135], v[134:135], s[38:39], v[158:159] op_sel_hi:[1,0,1]
	v_pk_fma_f32 v[130:131], v[130:131], s[38:39], v[154:155] op_sel_hi:[1,0,1]
	v_pk_fma_f32 v[136:137], v[136:137], s[38:39], v[156:157] op_sel_hi:[1,0,1]
	v_pk_mul_f32 v[134:135], v[4:5], v[134:135] op_sel_hi:[0,1]
	v_pk_fma_f32 v[132:133], v[132:133], s[38:39], v[152:153] op_sel_hi:[1,0,1]
	v_pk_mul_f32 v[130:131], v[4:5], v[130:131] op_sel_hi:[0,1]
	v_lshlrev_b32_e32 v150, 16, v2
	v_and_b32_e32 v151, 0xffff0000, v2
	v_lshlrev_b32_e32 v8, 16, v3
	v_and_b32_e32 v9, 0xffff0000, v3
	v_lshlrev_b32_e32 v2, 16, v5
	v_and_b32_e32 v3, 0xffff0000, v5
	v_pk_mul_f32 v[136:137], v[4:5], v[136:137] op_sel_hi:[0,1]
	v_pk_mul_f32 v[132:133], v[4:5], v[132:133] op_sel_hi:[0,1]
	v_med3_f32 v5, v134, s75, v164
	v_med3_f32 v134, v130, s75, v164
	v_med3_f32 v135, v135, s75, v164
	v_mov_b32_e32 v130, 0
	v_cvt_pk_fp8_f32 v130, v5, v135
	v_med3_f32 v136, v136, s75, v164
	v_med3_f32 v5, v137, s75, v164
	v_pk_fma_f32 v[126:127], v[126:127], s[38:39], v[150:151] op_sel_hi:[1,0,1]
	v_pk_fma_f32 v[128:129], v[128:129], s[38:39], v[8:9] op_sel_hi:[1,0,1]
	v_pk_fma_f32 v[122:123], v[122:123], s[38:39], v[6:7] op_sel_hi:[1,0,1]
	v_pk_fma_f32 v[124:125], v[124:125], s[38:39], v[2:3] op_sel_hi:[1,0,1]
	v_cvt_pk_fp8_f32 v130, v136, v5 op_sel:[0,0,1]
	v_pk_mul_f32 v[128:129], v[4:5], v[128:129] op_sel_hi:[0,1]
	v_pk_mul_f32 v[126:127], v[4:5], v[126:127] op_sel_hi:[0,1]
	v_pk_mul_f32 v[124:125], v[4:5], v[124:125] op_sel_hi:[0,1]
	v_pk_mul_f32 v[4:5], v[4:5], v[122:123] op_sel_hi:[0,1]
	v_med3_f32 v146, v131, s75, v164
	v_mov_b32_e32 v131, 0
	v_med3_f32 v122, v126, s75, v164
	v_med3_f32 v123, v4, s75, v164
	v_med3_f32 v126, v127, s75, v164
	v_med3_f32 v127, v5, s75, v164
	v_mov_b32_e32 v4, 0
	v_mov_b32_e32 v5, 0
	v_cvt_pk_fp8_f32 v131, v134, v146
	v_cvt_pk_fp8_f32 v4, v122, v126
	v_cvt_pk_fp8_f32 v5, v123, v127
	v_mov_b32_e32 v171, v0
	v_med3_f32 v132, v132, s75, v164
	v_readfirstlane_b32 s41, v171
	s_lshr_b32 s8, s41, 6
	v_med3_f32 v133, v133, s75, v164
	v_med3_f32 v128, v128, s75, v164
	v_med3_f32 v124, v124, s75, v164
	v_med3_f32 v122, v129, s75, v164
	v_med3_f32 v123, v125, s75, v164
	s_mulk_i32 s8, 0xb00
	v_cvt_pk_fp8_f32 v131, v132, v133 op_sel:[0,0,1]
	v_cvt_pk_fp8_f32 v4, v128, v122 op_sel:[0,0,1]
	v_cvt_pk_fp8_f32 v5, v124, v123 op_sel:[0,0,1]
	s_add_i32 s8, s8, 0
	v_and_b32_e32 v172, 15, v171
	v_lshrrev_b32_e32 v123, 1, v171
	s_add_i32 s43, s8, 0x20000
	v_mul_u32_u24_e32 v122, 0x50, v172
	v_and_b32_e32 v123, 24, v123
	v_add3_u32 v122, s43, v122, v123
	s_and_b32 s9, s41, 0xc0
	ds_write2_b64 v122, v[130:131], v[4:5] offset1:4
	v_bfe_u32 v4, v171, 2, 4
	s_ashr_i32 s41, s41, 2
	v_mul_u32_u24_e32 v5, 0x50, v4
	v_lshlrev_b32_e32 v123, 4, v171
	s_andn2_b32 s41, s41, 63
	v_lshl_or_b32 v4, s50, 8, v4
	v_and_b32_e32 v146, 48, v123
	v_add_u32_e32 v4, s41, v4
	v_mul_f32_e32 v130, 0x41000000, v170
	v_pk_fma_f32 v[118:119], v[118:119], s[38:39], v[158:159] op_sel_hi:[1,0,1]
	v_pk_fma_f32 v[114:115], v[114:115], s[38:39], v[154:155] op_sel_hi:[1,0,1]
	v_add3_u32 v123, s43, v5, v146
	v_ashrrev_i32_e32 v5, 31, v4
	v_pk_mul_f32 v[118:119], v[130:131], v[118:119] op_sel_hi:[0,1]
	v_pk_mul_f32 v[114:115], v[130:131], v[114:115] op_sel_hi:[0,1]
	v_lshlrev_b64 v[128:129], 10, v[4:5]
	v_med3_f32 v5, v118, s75, v164
	v_med3_f32 v118, v114, s75, v164
	v_med3_f32 v119, v119, s75, v164
	v_mov_b32_e32 v114, v147
	v_cvt_pk_fp8_f32 v114, v5, v119
	v_pk_fma_f32 v[120:121], v[120:121], s[38:39], v[156:157] op_sel_hi:[1,0,1]
	v_pk_fma_f32 v[116:117], v[116:117], s[38:39], v[152:153] op_sel_hi:[1,0,1]
	v_pk_mul_f32 v[120:121], v[130:131], v[120:121] op_sel_hi:[0,1]
	v_pk_mul_f32 v[116:117], v[130:131], v[116:117] op_sel_hi:[0,1]
	v_med3_f32 v131, v115, s75, v164
	v_pk_fma_f32 v[110:111], v[110:111], s[38:39], v[150:151] op_sel_hi:[1,0,1]
	v_pk_fma_f32 v[106:107], v[106:107], s[38:39], v[6:7] op_sel_hi:[1,0,1]
	v_med3_f32 v120, v120, s75, v164
	v_med3_f32 v5, v121, s75, v164
	v_pk_mul_f32 v[110:111], v[130:131], v[110:111] op_sel_hi:[0,1]
	v_pk_mul_f32 v[106:107], v[130:131], v[106:107] op_sel_hi:[0,1]
	v_cvt_pk_fp8_f32 v114, v120, v5 op_sel:[0,0,1]
	v_med3_f32 v5, v110, s75, v164
	v_med3_f32 v110, v106, s75, v164
	v_med3_f32 v111, v111, s75, v164
	v_mov_b32_e32 v106, v147
	v_cvt_pk_fp8_f32 v106, v5, v111
	v_pk_fma_f32 v[112:113], v[112:113], s[38:39], v[8:9] op_sel_hi:[1,0,1]
	v_mov_b32_e32 v115, v147
	v_pk_mul_f32 v[112:113], v[130:131], v[112:113] op_sel_hi:[0,1]
	v_med3_f32 v112, v112, s75, v164
	v_med3_f32 v5, v113, s75, v164
	v_cvt_pk_fp8_f32 v106, v112, v5 op_sel:[0,0,1]
	v_mul_f32_e32 v112, 0x41000000, v169
	v_pk_fma_f32 v[102:103], v[102:103], s[38:39], v[158:159] op_sel_hi:[1,0,1]
	v_pk_fma_f32 v[98:99], v[98:99], s[38:39], v[154:155] op_sel_hi:[1,0,1]
	v_cvt_pk_fp8_f32 v115, v118, v131
	v_pk_mul_f32 v[102:103], v[112:113], v[102:103] op_sel_hi:[0,1]
	v_pk_mul_f32 v[98:99], v[112:113], v[98:99] op_sel_hi:[0,1]
	v_med3_f32 v5, v102, s75, v164
	v_med3_f32 v102, v98, s75, v164
	v_med3_f32 v103, v103, s75, v164
	v_mov_b32_e32 v98, v147
	v_cvt_pk_fp8_f32 v98, v5, v103
	v_med3_f32 v116, v116, s75, v164
	v_med3_f32 v117, v117, s75, v164
	v_pk_fma_f32 v[104:105], v[104:105], s[38:39], v[156:157] op_sel_hi:[1,0,1]
	v_pk_fma_f32 v[100:101], v[100:101], s[38:39], v[152:153] op_sel_hi:[1,0,1]
	v_cvt_pk_fp8_f32 v115, v116, v117 op_sel:[0,0,1]
	v_med3_f32 v116, v107, s75, v164
	v_mov_b32_e32 v107, v147
	v_pk_mul_f32 v[104:105], v[112:113], v[104:105] op_sel_hi:[0,1]
	v_pk_mul_f32 v[100:101], v[112:113], v[100:101] op_sel_hi:[0,1]
	v_med3_f32 v113, v99, s75, v164
	v_pk_fma_f32 v[94:95], v[94:95], s[38:39], v[150:151] op_sel_hi:[1,0,1]
	v_pk_fma_f32 v[90:91], v[90:91], s[38:39], v[6:7] op_sel_hi:[1,0,1]
	v_cvt_pk_fp8_f32 v107, v110, v116
	v_med3_f32 v104, v104, s75, v164
	v_med3_f32 v5, v105, s75, v164
	v_pk_mul_f32 v[94:95], v[112:113], v[94:95] op_sel_hi:[0,1]
	v_pk_mul_f32 v[90:91], v[112:113], v[90:91] op_sel_hi:[0,1]
	v_pk_fma_f32 v[108:109], v[108:109], s[38:39], v[2:3] op_sel_hi:[1,0,1]
	v_mov_b32_e32 v99, v147
	v_cvt_pk_fp8_f32 v98, v104, v5 op_sel:[0,0,1]
	v_med3_f32 v5, v94, s75, v164
	v_med3_f32 v94, v90, s75, v164
	v_med3_f32 v95, v95, s75, v164
	v_mov_b32_e32 v90, v147
	s_lshl_b32 s8, s62, 8
	ds_read_b128 v[124:127], v123
	v_pk_mul_f32 v[108:109], v[130:131], v[108:109] op_sel_hi:[0,1]
	v_cvt_pk_fp8_f32 v99, v102, v113
	v_cvt_pk_fp8_f32 v90, v5, v95
	s_or_b32 s8, s9, s8
	v_med3_f32 v108, v108, s75, v164
	v_med3_f32 v109, v109, s75, v164
	v_pk_fma_f32 v[96:97], v[96:97], s[38:39], v[8:9] op_sel_hi:[1,0,1]
	s_ashr_i32 s9, s8, 31
	v_lshl_add_u64 v[128:129], s[16:17], 0, v[128:129]
	v_cvt_pk_fp8_f32 v107, v108, v109 op_sel:[0,0,1]
	v_pk_mul_f32 v[96:97], v[112:113], v[96:97] op_sel_hi:[0,1]
	v_lshl_add_u64 v[128:129], v[128:129], 0, s[8:9]
	v_med3_f32 v100, v100, s75, v164
	v_med3_f32 v101, v101, s75, v164
	v_med3_f32 v96, v96, s75, v164
	v_med3_f32 v5, v97, s75, v164
	v_lshl_add_u64 v[108:109], v[128:129], 0, v[146:147]
	v_cvt_pk_fp8_f32 v99, v100, v101 op_sel:[0,0,1]
	v_med3_f32 v100, v91, s75, v164
	v_mov_b32_e32 v91, v147
	v_cvt_pk_fp8_f32 v90, v96, v5 op_sel:[0,0,1]
	v_mul_f32_e32 v96, 0x41000000, v168
	v_pk_fma_f32 v[78:79], v[78:79], s[38:39], v[158:159] op_sel_hi:[1,0,1]
	v_pk_fma_f32 v[74:75], v[74:75], s[38:39], v[154:155] op_sel_hi:[1,0,1]
	s_waitcnt lgkmcnt(0)
	global_store_dwordx4 v[108:109], v[124:127], off
	v_cvt_pk_fp8_f32 v91, v94, v100
	v_pk_fma_f32 v[80:81], v[80:81], s[38:39], v[156:157] op_sel_hi:[1,0,1]
	v_pk_mul_f32 v[78:79], v[96:97], v[78:79] op_sel_hi:[0,1]
	v_pk_fma_f32 v[76:77], v[76:77], s[38:39], v[152:153] op_sel_hi:[1,0,1]
	v_pk_mul_f32 v[74:75], v[96:97], v[74:75] op_sel_hi:[0,1]
	ds_write2_b64 v122, v[114:115], v[106:107] offset1:4
	v_or_b32_e32 v110, 16, v4
	v_pk_fma_f32 v[92:93], v[92:93], s[38:39], v[2:3] op_sel_hi:[1,0,1]
	v_pk_mul_f32 v[80:81], v[96:97], v[80:81] op_sel_hi:[0,1]
	v_pk_mul_f32 v[76:77], v[96:97], v[76:77] op_sel_hi:[0,1]
	v_med3_f32 v5, v78, s75, v164
	v_med3_f32 v78, v74, s75, v164
	v_med3_f32 v79, v79, s75, v164
	v_med3_f32 v97, v75, s75, v164
	v_mov_b32_e32 v74, v147
	v_mov_b32_e32 v75, v147
	ds_read_b128 v[106:109], v123
	v_ashrrev_i32_e32 v111, 31, v110
	v_pk_mul_f32 v[92:93], v[112:113], v[92:93] op_sel_hi:[0,1]
	v_cvt_pk_fp8_f32 v74, v5, v79
	v_cvt_pk_fp8_f32 v75, v78, v97
	v_lshlrev_b64 v[110:111], 10, v[110:111]
	v_med3_f32 v92, v92, s75, v164
	v_med3_f32 v93, v93, s75, v164
	v_lshl_add_u64 v[110:111], s[16:17], 0, v[110:111]
	v_cvt_pk_fp8_f32 v91, v92, v93 op_sel:[0,0,1]
	v_pk_fma_f32 v[62:63], v[62:63], s[38:39], v[150:151] op_sel_hi:[1,0,1]
	v_pk_fma_f32 v[58:59], v[58:59], s[38:39], v[6:7] op_sel_hi:[1,0,1]
	v_lshl_add_u64 v[110:111], v[110:111], 0, s[8:9]
	v_med3_f32 v80, v80, s75, v164
	v_med3_f32 v76, v76, s75, v164
	v_med3_f32 v5, v81, s75, v164
	v_med3_f32 v77, v77, s75, v164
	v_pk_mul_f32 v[62:63], v[96:97], v[62:63] op_sel_hi:[0,1]
	v_pk_mul_f32 v[58:59], v[96:97], v[58:59] op_sel_hi:[0,1]
	v_lshl_add_u64 v[92:93], v[110:111], 0, v[146:147]
	v_cvt_pk_fp8_f32 v74, v80, v5 op_sel:[0,0,1]
	v_cvt_pk_fp8_f32 v75, v76, v77 op_sel:[0,0,1]
	v_med3_f32 v5, v62, s75, v164
	v_med3_f32 v62, v58, s75, v164
	v_med3_f32 v63, v63, s75, v164
	v_med3_f32 v76, v59, s75, v164
	v_mov_b32_e32 v58, v147
	v_mov_b32_e32 v59, v147
	s_waitcnt lgkmcnt(0)
	global_store_dwordx4 v[92:93], v[106:109], off
	v_cvt_pk_fp8_f32 v58, v5, v63
	v_cvt_pk_fp8_f32 v59, v62, v76
	ds_write2_b64 v122, v[98:99], v[90:91] offset1:4
	v_or_b32_e32 v94, 32, v4
	v_pk_fma_f32 v[64:65], v[64:65], s[38:39], v[8:9] op_sel_hi:[1,0,1]
	v_pk_fma_f32 v[60:61], v[60:61], s[38:39], v[2:3] op_sel_hi:[1,0,1]
	ds_read_b128 v[90:93], v123
	v_ashrrev_i32_e32 v95, 31, v94
	v_pk_mul_f32 v[64:65], v[96:97], v[64:65] op_sel_hi:[0,1]
	v_pk_mul_f32 v[60:61], v[96:97], v[60:61] op_sel_hi:[0,1]
	v_lshlrev_b64 v[94:95], 10, v[94:95]
	v_med3_f32 v64, v64, s75, v164
	v_med3_f32 v60, v60, s75, v164
	v_med3_f32 v5, v65, s75, v164
	v_med3_f32 v61, v61, s75, v164
	v_lshl_add_u64 v[94:95], s[16:17], 0, v[94:95]
	v_cvt_pk_fp8_f32 v58, v64, v5 op_sel:[0,0,1]
	v_cvt_pk_fp8_f32 v59, v60, v61 op_sel:[0,0,1]
	v_lshl_add_u64 v[94:95], v[94:95], 0, s[8:9]
	v_lshl_add_u64 v[60:61], v[94:95], 0, v[146:147]
	s_waitcnt lgkmcnt(0)
	global_store_dwordx4 v[60:61], v[90:93], off
	ds_write2_b64 v122, v[74:75], v[58:59] offset1:4
	v_mul_f32_e32 v64, 0x41000000, v167
	v_pk_fma_f32 v[74:75], v[86:87], s[38:39], v[158:159] op_sel_hi:[1,0,1]
	v_pk_fma_f32 v[78:79], v[82:83], s[38:39], v[154:155] op_sel_hi:[1,0,1]
	v_pk_mul_f32 v[74:75], v[64:65], v[74:75] op_sel_hi:[0,1]
	v_pk_fma_f32 v[76:77], v[88:89], s[38:39], v[156:157] op_sel_hi:[1,0,1]
	v_pk_fma_f32 v[80:81], v[84:85], s[38:39], v[152:153] op_sel_hi:[1,0,1]
	v_pk_mul_f32 v[78:79], v[64:65], v[78:79] op_sel_hi:[0,1]
	v_med3_f32 v5, v74, s75, v164
	v_med3_f32 v75, v75, s75, v164
	v_mov_b32_e32 v74, v147
	v_pk_mul_f32 v[76:77], v[64:65], v[76:77] op_sel_hi:[0,1]
	v_pk_mul_f32 v[80:81], v[64:65], v[80:81] op_sel_hi:[0,1]
	v_med3_f32 v65, v78, s75, v164
	v_med3_f32 v78, v79, s75, v164
	v_cvt_pk_fp8_f32 v74, v5, v75
	v_mov_b32_e32 v75, v147
	v_cvt_pk_fp8_f32 v75, v65, v78
	v_med3_f32 v79, v80, s75, v164
	v_med3_f32 v65, v81, s75, v164
	v_pk_fma_f32 v[70:71], v[70:71], s[38:39], v[150:151] op_sel_hi:[1,0,1]
	v_pk_fma_f32 v[72:73], v[72:73], s[38:39], v[8:9] op_sel_hi:[1,0,1]
	v_pk_fma_f32 v[66:67], v[66:67], s[38:39], v[6:7] op_sel_hi:[1,0,1]
	v_pk_fma_f32 v[68:69], v[68:69], s[38:39], v[2:3] op_sel_hi:[1,0,1]
	v_med3_f32 v76, v76, s75, v164
	v_med3_f32 v5, v77, s75, v164
	v_cvt_pk_fp8_f32 v75, v79, v65 op_sel:[0,0,1]
	v_pk_mul_f32 v[72:73], v[64:65], v[72:73] op_sel_hi:[0,1]
	v_pk_mul_f32 v[70:71], v[64:65], v[70:71] op_sel_hi:[0,1]
	v_pk_mul_f32 v[68:69], v[64:65], v[68:69] op_sel_hi:[0,1]
	v_pk_mul_f32 v[64:65], v[64:65], v[66:67] op_sel_hi:[0,1]
	v_cvt_pk_fp8_f32 v74, v76, v5 op_sel:[0,0,1]
	v_med3_f32 v5, v70, s75, v164
	v_med3_f32 v66, v64, s75, v164
	v_med3_f32 v67, v71, s75, v164
	v_med3_f32 v70, v65, s75, v164
	v_mov_b32_e32 v64, v147
	v_mov_b32_e32 v65, v147
	v_cvt_pk_fp8_f32 v64, v5, v67
	v_cvt_pk_fp8_f32 v65, v66, v70
	v_or_b32_e32 v62, 48, v4
	ds_read_b128 v[58:61], v123
	v_ashrrev_i32_e32 v63, 31, v62
	v_lshlrev_b64 v[62:63], 10, v[62:63]
	v_med3_f32 v71, v72, s75, v164
	v_med3_f32 v68, v68, s75, v164
	v_med3_f32 v5, v73, s75, v164
	v_med3_f32 v66, v69, s75, v164
	v_lshl_add_u64 v[62:63], s[16:17], 0, v[62:63]
	v_cvt_pk_fp8_f32 v64, v71, v5 op_sel:[0,0,1]
	v_cvt_pk_fp8_f32 v65, v68, v66 op_sel:[0,0,1]
	v_lshl_add_u64 v[62:63], v[62:63], 0, s[8:9]
	v_lshl_add_u64 v[62:63], v[62:63], 0, v[146:147]
	s_waitcnt lgkmcnt(0)
	global_store_dwordx4 v[62:63], v[58:61], off
	ds_write2_b64 v122, v[74:75], v[64:65] offset1:4
	v_mul_f32_e32 v64, 0x41000000, v166
	v_pk_fma_f32 v[54:55], v[54:55], s[38:39], v[158:159] op_sel_hi:[1,0,1]
	v_pk_fma_f32 v[50:51], v[50:51], s[38:39], v[154:155] op_sel_hi:[1,0,1]
	v_pk_mul_f32 v[54:55], v[64:65], v[54:55] op_sel_hi:[0,1]
	v_pk_mul_f32 v[50:51], v[64:65], v[50:51] op_sel_hi:[0,1]
	v_med3_f32 v5, v54, s75, v164
	v_med3_f32 v54, v50, s75, v164
	v_med3_f32 v55, v55, s75, v164
	v_mov_b32_e32 v50, v147
	v_cvt_pk_fp8_f32 v50, v5, v55
	v_pk_fma_f32 v[56:57], v[56:57], s[38:39], v[156:157] op_sel_hi:[1,0,1]
	v_pk_fma_f32 v[52:53], v[52:53], s[38:39], v[152:153] op_sel_hi:[1,0,1]
	v_pk_mul_f32 v[56:57], v[64:65], v[56:57] op_sel_hi:[0,1]
	v_pk_mul_f32 v[52:53], v[64:65], v[52:53] op_sel_hi:[0,1]
	v_med3_f32 v65, v51, s75, v164
	v_pk_fma_f32 v[46:47], v[46:47], s[38:39], v[150:151] op_sel_hi:[1,0,1]
	v_pk_fma_f32 v[42:43], v[42:43], s[38:39], v[6:7] op_sel_hi:[1,0,1]
	v_med3_f32 v56, v56, s75, v164
	v_med3_f32 v5, v57, s75, v164
	v_pk_mul_f32 v[46:47], v[64:65], v[46:47] op_sel_hi:[0,1]
	v_pk_mul_f32 v[42:43], v[64:65], v[42:43] op_sel_hi:[0,1]
	v_cvt_pk_fp8_f32 v50, v56, v5 op_sel:[0,0,1]
	v_med3_f32 v5, v46, s75, v164
	v_med3_f32 v46, v42, s75, v164
	v_med3_f32 v47, v47, s75, v164
	v_mov_b32_e32 v42, v147
	v_cvt_pk_fp8_f32 v42, v5, v47
	v_pk_fma_f32 v[48:49], v[48:49], s[38:39], v[8:9] op_sel_hi:[1,0,1]
	v_mov_b32_e32 v51, v147
	v_pk_mul_f32 v[48:49], v[64:65], v[48:49] op_sel_hi:[0,1]
	v_med3_f32 v48, v48, s75, v164
	v_med3_f32 v5, v49, s75, v164
	v_cvt_pk_fp8_f32 v42, v48, v5 op_sel:[0,0,1]
	v_mul_f32_e32 v48, 0x41000000, v165
	v_pk_fma_f32 v[38:39], v[38:39], s[38:39], v[158:159] op_sel_hi:[1,0,1]
	v_pk_fma_f32 v[34:35], v[34:35], s[38:39], v[154:155] op_sel_hi:[1,0,1]
	v_cvt_pk_fp8_f32 v51, v54, v65
	v_pk_mul_f32 v[38:39], v[48:49], v[38:39] op_sel_hi:[0,1]
	v_pk_mul_f32 v[34:35], v[48:49], v[34:35] op_sel_hi:[0,1]
	v_med3_f32 v5, v38, s75, v164
	v_med3_f32 v38, v34, s75, v164
	v_med3_f32 v39, v39, s75, v164
	v_mov_b32_e32 v34, v147
	v_cvt_pk_fp8_f32 v34, v5, v39
	v_med3_f32 v52, v52, s75, v164
	v_med3_f32 v53, v53, s75, v164
	v_pk_fma_f32 v[40:41], v[40:41], s[38:39], v[156:157] op_sel_hi:[1,0,1]
	v_pk_fma_f32 v[36:37], v[36:37], s[38:39], v[152:153] op_sel_hi:[1,0,1]
	v_cvt_pk_fp8_f32 v51, v52, v53 op_sel:[0,0,1]
	v_med3_f32 v52, v43, s75, v164
	v_mov_b32_e32 v43, v147
	v_pk_mul_f32 v[40:41], v[48:49], v[40:41] op_sel_hi:[0,1]
	v_pk_mul_f32 v[36:37], v[48:49], v[36:37] op_sel_hi:[0,1]
	v_med3_f32 v49, v35, s75, v164
	v_pk_fma_f32 v[30:31], v[30:31], s[38:39], v[150:151] op_sel_hi:[1,0,1]
	v_pk_fma_f32 v[26:27], v[26:27], s[38:39], v[6:7] op_sel_hi:[1,0,1]
	v_cvt_pk_fp8_f32 v43, v46, v52
	v_med3_f32 v40, v40, s75, v164
	v_med3_f32 v5, v41, s75, v164
	v_pk_mul_f32 v[30:31], v[48:49], v[30:31] op_sel_hi:[0,1]
	v_pk_mul_f32 v[26:27], v[48:49], v[26:27] op_sel_hi:[0,1]
	v_add_u32_e32 v62, 0x80, v4
	v_pk_fma_f32 v[44:45], v[44:45], s[38:39], v[2:3] op_sel_hi:[1,0,1]
	v_mov_b32_e32 v35, v147
	v_cvt_pk_fp8_f32 v34, v40, v5 op_sel:[0,0,1]
	v_med3_f32 v5, v30, s75, v164
	v_med3_f32 v30, v26, s75, v164
	v_med3_f32 v31, v31, s75, v164
	v_mov_b32_e32 v26, v147
	ds_read_b128 v[58:61], v123
	v_ashrrev_i32_e32 v63, 31, v62
	v_pk_mul_f32 v[44:45], v[64:65], v[44:45] op_sel_hi:[0,1]
	v_cvt_pk_fp8_f32 v35, v38, v49
	v_cvt_pk_fp8_f32 v26, v5, v31
	v_lshlrev_b64 v[62:63], 10, v[62:63]
	v_med3_f32 v44, v44, s75, v164
	v_med3_f32 v45, v45, s75, v164
	v_pk_fma_f32 v[32:33], v[32:33], s[38:39], v[8:9] op_sel_hi:[1,0,1]
	v_lshl_add_u64 v[62:63], s[16:17], 0, v[62:63]
	v_cvt_pk_fp8_f32 v43, v44, v45 op_sel:[0,0,1]
	v_pk_mul_f32 v[32:33], v[48:49], v[32:33] op_sel_hi:[0,1]
	v_lshl_add_u64 v[62:63], v[62:63], 0, s[8:9]
	v_med3_f32 v36, v36, s75, v164
	v_med3_f32 v37, v37, s75, v164
	v_med3_f32 v32, v32, s75, v164
	v_med3_f32 v5, v33, s75, v164
	v_lshl_add_u64 v[44:45], v[62:63], 0, v[146:147]
	v_cvt_pk_fp8_f32 v35, v36, v37 op_sel:[0,0,1]
	v_med3_f32 v36, v27, s75, v164
	v_mov_b32_e32 v27, v147
	v_cvt_pk_fp8_f32 v26, v32, v5 op_sel:[0,0,1]
	v_mul_f32_e32 v32, 0x41000000, v1
	v_pk_fma_f32 v[22:23], v[22:23], s[38:39], v[158:159] op_sel_hi:[1,0,1]
	v_pk_fma_f32 v[18:19], v[18:19], s[38:39], v[154:155] op_sel_hi:[1,0,1]
	s_waitcnt lgkmcnt(0)
	global_store_dwordx4 v[44:45], v[58:61], off
	v_cvt_pk_fp8_f32 v27, v30, v36
	v_pk_mul_f32 v[22:23], v[32:33], v[22:23] op_sel_hi:[0,1]
	v_pk_mul_f32 v[18:19], v[32:33], v[18:19] op_sel_hi:[0,1]
	ds_write2_b64 v122, v[50:51], v[42:43] offset1:4
	v_add_u32_e32 v46, 0x90, v4
	v_pk_fma_f32 v[28:29], v[28:29], s[38:39], v[2:3] op_sel_hi:[1,0,1]
	v_med3_f32 v1, v22, s75, v164
	v_med3_f32 v5, v18, s75, v164
	v_med3_f32 v22, v23, s75, v164
	v_med3_f32 v23, v19, s75, v164
	v_mov_b32_e32 v18, v147
	v_mov_b32_e32 v19, v147
	ds_read_b128 v[42:45], v123
	v_ashrrev_i32_e32 v47, 31, v46
	v_pk_mul_f32 v[28:29], v[48:49], v[28:29] op_sel_hi:[0,1]
	v_cvt_pk_fp8_f32 v18, v1, v22
	v_cvt_pk_fp8_f32 v19, v5, v23
	v_lshlrev_b64 v[46:47], 10, v[46:47]
	v_med3_f32 v28, v28, s75, v164
	v_med3_f32 v29, v29, s75, v164
	v_pk_fma_f32 v[24:25], v[24:25], s[38:39], v[156:157] op_sel_hi:[1,0,1]
	v_pk_fma_f32 v[20:21], v[20:21], s[38:39], v[152:153] op_sel_hi:[1,0,1]
	v_lshl_add_u64 v[46:47], s[16:17], 0, v[46:47]
	v_cvt_pk_fp8_f32 v27, v28, v29 op_sel:[0,0,1]
	v_pk_mul_f32 v[24:25], v[32:33], v[24:25] op_sel_hi:[0,1]
	v_pk_mul_f32 v[20:21], v[32:33], v[20:21] op_sel_hi:[0,1]
	v_pk_fma_f32 v[14:15], v[14:15], s[38:39], v[150:151] op_sel_hi:[1,0,1]
	v_pk_fma_f32 v[6:7], v[10:11], s[38:39], v[6:7] op_sel_hi:[1,0,1]
	v_lshl_add_u64 v[46:47], v[46:47], 0, s[8:9]
	v_med3_f32 v24, v24, s75, v164
	v_med3_f32 v20, v20, s75, v164
	v_med3_f32 v1, v25, s75, v164
	v_med3_f32 v5, v21, s75, v164
	v_pk_mul_f32 v[14:15], v[32:33], v[14:15] op_sel_hi:[0,1]
	v_pk_mul_f32 v[6:7], v[32:33], v[6:7] op_sel_hi:[0,1]
	v_lshl_add_u64 v[28:29], v[46:47], 0, v[146:147]
	v_cvt_pk_fp8_f32 v18, v24, v1 op_sel:[0,0,1]
	v_cvt_pk_fp8_f32 v19, v20, v5 op_sel:[0,0,1]
	v_med3_f32 v1, v14, s75, v164
	v_med3_f32 v5, v6, s75, v164
	v_med3_f32 v10, v15, s75, v164
	v_med3_f32 v11, v7, s75, v164
	v_mov_b32_e32 v6, v147
	v_mov_b32_e32 v7, v147
	s_waitcnt lgkmcnt(0)
	global_store_dwordx4 v[28:29], v[42:45], off
	v_cvt_pk_fp8_f32 v6, v1, v10
	v_cvt_pk_fp8_f32 v7, v5, v11
	ds_write2_b64 v122, v[34:35], v[26:27] offset1:4
	v_add_u32_e32 v30, 0xa0, v4
	v_pk_fma_f32 v[8:9], v[16:17], s[38:39], v[8:9] op_sel_hi:[1,0,1]
	v_pk_fma_f32 v[2:3], v[12:13], s[38:39], v[2:3] op_sel_hi:[1,0,1]
	ds_read_b128 v[26:29], v123
	v_ashrrev_i32_e32 v31, 31, v30
	v_pk_mul_f32 v[8:9], v[32:33], v[8:9] op_sel_hi:[0,1]
	v_pk_mul_f32 v[2:3], v[32:33], v[2:3] op_sel_hi:[0,1]
	v_lshlrev_b64 v[30:31], 10, v[30:31]
	v_med3_f32 v8, v8, s75, v164
	v_med3_f32 v2, v2, s75, v164
	v_med3_f32 v1, v9, s75, v164
	v_med3_f32 v3, v3, s75, v164
	v_lshl_add_u64 v[30:31], s[16:17], 0, v[30:31]
	v_cvt_pk_fp8_f32 v6, v8, v1 op_sel:[0,0,1]
	v_cvt_pk_fp8_f32 v7, v2, v3 op_sel:[0,0,1]
	v_lshl_add_u64 v[30:31], v[30:31], 0, s[8:9]
	v_lshl_add_u64 v[2:3], v[30:31], 0, v[146:147]
	s_waitcnt lgkmcnt(0)
	global_store_dwordx4 v[2:3], v[26:29], off
	ds_write2_b64 v122, v[18:19], v[6:7] offset1:4
	v_add_u32_e32 v2, 0xb0, v4
	ds_read_b128 v[6:9], v123
	v_ashrrev_i32_e32 v3, 31, v2
	v_lshlrev_b64 v[2:3], 10, v[2:3]
	v_lshl_add_u64 v[2:3], s[16:17], 0, v[2:3]
	v_lshl_add_u64 v[2:3], v[2:3], 0, s[8:9]
	v_lshl_add_u64 v[2:3], v[2:3], 0, v[146:147]
	s_waitcnt lgkmcnt(0)
	global_store_dwordx4 v[2:3], v[6:9], off
	s_and_b64 vcc, exec, s[10:11]
	s_mov_b64 s[8:9], -1
	s_cbranch_vccnz .LBB0_3418
	v_mov_b32_e32 v12, v0
	s_lshl_b32 s9, s42, 8
	v_readfirstlane_b32 s8, v12
	s_and_b32 s10, s8, 0xc0
	s_ashr_i32 s8, s8, 2
	s_andn2_b32 s8, s8, 63
	s_add_i32 s8, s8, s9
	v_and_or_b32 v2, v12, 15, s8
	v_ashrrev_i32_e32 v3, 31, v2
	s_lshl_b64 s[8:9], s[44:45], 11
	v_lshl_add_u64 v[4:5], v[2:3], 2, s[12:13]
	v_add_u32_e32 v6, 0x80, v2
	v_add_u32_e32 v8, 0x90, v2
	v_add_u32_e32 v10, 0xa0, v2
	v_add_u32_e32 v2, 0xb0, v2
	s_add_u32 s11, s54, s8
	v_ashrrev_i32_e32 v7, 31, v6
	v_ashrrev_i32_e32 v9, 31, v8
	v_ashrrev_i32_e32 v11, 31, v10
	v_ashrrev_i32_e32 v3, 31, v2
	s_addc_u32 s41, s55, s9
	s_lshl_b32 s8, s40, 8
	v_lshl_add_u64 v[6:7], v[6:7], 2, s[12:13]
	v_lshl_add_u64 v[8:9], v[8:9], 2, s[12:13]
	v_lshl_add_u64 v[10:11], v[10:11], 2, s[12:13]
	v_lshl_add_u64 v[2:3], v[2:3], 2, s[12:13]
	global_load_dword v146, v[4:5], off
	global_load_dword v170, v[4:5], off offset:64
	global_load_dword v169, v[4:5], off offset:128
	global_load_dword v168, v[4:5], off offset:192
	global_load_dword v167, v[6:7], off
	global_load_dword v166, v[8:9], off
	global_load_dword v165, v[10:11], off
	global_load_dword v1, v[2:3], off
	s_ashr_i32 s9, s8, 31
	s_lshl_b64 s[8:9], s[8:9], 1
	s_add_u32 s8, s11, s8
	s_addc_u32 s9, s41, s9
	s_lshl_b32 s10, s10, 1
	s_add_u32 s8, s8, s10
	s_addc_u32 s9, s9, 0
	v_and_b32_e32 v2, 48, v12
	global_load_dwordx4 v[6:9], v2, s[8:9]
	s_nop 0
	global_load_dwordx4 v[2:5], v2, s[8:9] offset:64
	s_andn2_b64 vcc, exec, s[14:15]
	s_cbranch_vccnz .LBB0_3417
	s_barrier
	s_branch .LBB0_3417
